# nt hint also on the read-once input streams (ada_w in the prologue, f32 x/ctx rows in N1 layer 0)
# speedup vs baseline: 1.0167x; 1.0167x over previous
; #define GAS __attribute__((address_space(1)))
; #define MODW_LD(W, j0) do { _Pragma("unroll") for (int q = 0; q < 4; ++q) W[q] = *(const GAS f32x4*)(wp + (size_t)(((j0) + q) & 63) * 16 * 6144); } while (0)
; __device__ __forceinline__ void p0_prologue(const Frame& F0) {
;     ...
;             const int kg = F.tid / 24, cq = F.tid % 24;
;             f32x4 acc[17];
; #pragma unroll
;             for (int r = 0; r < 17; ++r) acc[r] = (f32x4){0.f, 0.f, 0.f, 0.f};
;             if (kg < 16) {
;                 const GAS float* wp = (const GAS float*)(inp(F, I_ADAW) + ((size_t)L * 1024 + kg) * 6144 + n0 + 4 * cq);
;                 f32x4 wa[4], wb[4];
;     ...
;                 MODW_LD(wa, 0);
.LBB0_11:
	s_and_b32 s39, s38, 63
	v_mov_b32_e32 v5, 0
	s_ashr_i32 s18, s38, 6
	s_mulk_i32 s39, 0x60
	v_mov_b32_e32 v4, v5
	v_mov_b32_e32 v3, v5
	v_mov_b32_e32 v2, v5
	v_mov_b32_e32 v9, v5
	v_mov_b32_e32 v8, v5
	v_mov_b32_e32 v7, v5
	v_mov_b32_e32 v6, v5
	v_mov_b32_e32 v25, v5
	v_mov_b32_e32 v24, v5
	v_mov_b32_e32 v23, v5
	v_mov_b32_e32 v22, v5
	v_mov_b32_e32 v13, v5
	v_mov_b32_e32 v12, v5
	v_mov_b32_e32 v11, v5
	v_mov_b32_e32 v10, v5
	v_mov_b32_e32 v85, v5
	v_mov_b32_e32 v84, v5
	v_mov_b32_e32 v83, v5
	v_mov_b32_e32 v82, v5
	v_mov_b32_e32 v65, v5
	v_mov_b32_e32 v64, v5
	v_mov_b32_e32 v63, v5
	v_mov_b32_e32 v62, v5
	v_mov_b32_e32 v81, v5
	v_mov_b32_e32 v80, v5
	v_mov_b32_e32 v79, v5
	v_mov_b32_e32 v78, v5
	v_mov_b32_e32 v61, v5
	v_mov_b32_e32 v60, v5
	v_mov_b32_e32 v59, v5
	v_mov_b32_e32 v58, v5
	v_mov_b32_e32 v77, v5
	v_mov_b32_e32 v76, v5
	v_mov_b32_e32 v75, v5
	v_mov_b32_e32 v74, v5
	v_mov_b32_e32 v57, v5
	v_mov_b32_e32 v56, v5
	v_mov_b32_e32 v55, v5
	v_mov_b32_e32 v54, v5
	v_mov_b32_e32 v73, v5
	v_mov_b32_e32 v72, v5
	v_mov_b32_e32 v71, v5
	v_mov_b32_e32 v70, v5
	v_mov_b32_e32 v53, v5
	v_mov_b32_e32 v52, v5
	v_mov_b32_e32 v51, v5
	v_mov_b32_e32 v50, v5
	v_mov_b32_e32 v69, v5
	v_mov_b32_e32 v68, v5
	v_mov_b32_e32 v67, v5
	v_mov_b32_e32 v66, v5
	v_mov_b32_e32 v21, v5
	v_mov_b32_e32 v20, v5
	v_mov_b32_e32 v19, v5
	v_mov_b32_e32 v18, v5
	v_mov_b32_e32 v33, v5
	v_mov_b32_e32 v32, v5
	v_mov_b32_e32 v31, v5
	v_mov_b32_e32 v30, v5
	v_mov_b32_e32 v17, v5
	v_mov_b32_e32 v16, v5
	v_mov_b32_e32 v15, v5
	v_mov_b32_e32 v14, v5
	v_mov_b32_e32 v29, v5
	v_mov_b32_e32 v28, v5
	v_mov_b32_e32 v27, v5
	v_mov_b32_e32 v26, v5
	s_and_saveexec_b64 s[20:21], s[0:1]
	s_cbranch_execz .LBB0_14
	v_mov_b32_e32 v2, s28
	ds_read_b64 v[2:3], v2
	s_ashr_i32 s19, s18, 31
	s_lshl_b64 s[2:3], s[18:19], 10
	v_lshl_add_u64 v[4:5], s[2:3], 0, v[104:105]
	s_lshl_b32 s12, s39, 2
	s_waitcnt lgkmcnt(0)
	v_readfirstlane_b32 s8, v2
	v_readfirstlane_b32 s9, v3
	v_mov_b32_e32 v26, 0
	v_mov_b32_e32 v2, s8
	v_mov_b32_e32 v3, s9
	v_mad_u64_u32 v[2:3], s[2:3], v4, s22, v[2:3]
	v_mad_i32_i24 v3, v5, s22, v3
	v_lshl_add_u64 v[2:3], v[2:3], 0, s[12:13]
	v_lshl_add_u64 v[108:109], v[106:107], 2, v[2:3]
	v_add_co_u32_e32 v2, vcc, s29, v108
	s_mov_b32 s2, -8
	s_nop 0
	v_addc_co_u32_e32 v3, vcc, 0, v109, vcc
	v_add_co_u32_e32 v4, vcc, 0xc0000, v108
	v_mov_b32_e32 v27, v26
	s_nop 0
	v_addc_co_u32_e32 v5, vcc, 0, v109, vcc
	v_add_co_u32_e32 v6, vcc, 0x120000, v108
	v_mov_b32_e32 v28, v26
	s_nop 0
	v_addc_co_u32_e32 v7, vcc, 0, v109, vcc
	global_load_dwordx4 v[42:45], v[4:5], off nt
	global_load_dwordx4 v[34:37], v[6:7], off nt
	global_load_dwordx4 v[46:49], v[2:3], off nt
	global_load_dwordx4 v[38:41], v[108:109], off nt
	v_mov_b32_e32 v29, v26
	v_mov_b32_e32 v14, v26
	v_mov_b32_e32 v15, v26
	v_mov_b32_e32 v16, v26
	v_mov_b32_e32 v17, v26
	v_mov_b32_e32 v30, v26
	v_mov_b32_e32 v31, v26
	v_mov_b32_e32 v32, v26
	v_mov_b32_e32 v33, v26
	v_mov_b32_e32 v18, v26
	v_mov_b32_e32 v19, v26
	v_mov_b32_e32 v20, v26
	v_mov_b32_e32 v21, v26
	v_mov_b32_e32 v66, v26
	v_mov_b32_e32 v67, v26
	v_mov_b32_e32 v68, v26
	v_mov_b32_e32 v69, v26
	v_mov_b32_e32 v50, v26
	v_mov_b32_e32 v51, v26
	v_mov_b32_e32 v52, v26
	v_mov_b32_e32 v53, v26
	v_mov_b32_e32 v70, v26
	v_mov_b32_e32 v71, v26
	v_mov_b32_e32 v72, v26
	v_mov_b32_e32 v73, v26
	v_mov_b32_e32 v54, v26
	v_mov_b32_e32 v55, v26
	v_mov_b32_e32 v56, v26
	v_mov_b32_e32 v57, v26
	v_mov_b32_e32 v74, v26
	v_mov_b32_e32 v75, v26
	v_mov_b32_e32 v76, v26
	v_mov_b32_e32 v77, v26
	v_mov_b32_e32 v58, v26
	v_mov_b32_e32 v59, v26
	v_mov_b32_e32 v60, v26
	v_mov_b32_e32 v61, v26
	v_mov_b32_e32 v78, v26
	v_mov_b32_e32 v79, v26
	v_mov_b32_e32 v80, v26
	v_mov_b32_e32 v81, v26
	v_mov_b32_e32 v62, v26
	v_mov_b32_e32 v63, v26
	v_mov_b32_e32 v64, v26
	v_mov_b32_e32 v65, v26
	v_mov_b32_e32 v82, v26
	v_mov_b32_e32 v83, v26
	v_mov_b32_e32 v84, v26
	v_mov_b32_e32 v85, v26
	v_mov_b32_e32 v10, v26
	v_mov_b32_e32 v11, v26
	v_mov_b32_e32 v12, v26
	v_mov_b32_e32 v13, v26
	v_mov_b32_e32 v22, v26
	v_mov_b32_e32 v23, v26
	v_mov_b32_e32 v24, v26
	v_mov_b32_e32 v25, v26
	v_mov_b32_e32 v6, v26
	v_mov_b32_e32 v7, v26
	v_mov_b32_e32 v8, v26
	v_mov_b32_e32 v9, v26
	v_mov_b32_e32 v2, v26
	v_mov_b32_e32 v3, v26
	v_mov_b32_e32 v4, v26
	v_mov_b32_e32 v5, v26
	v_mov_b32_e32 v131, v1
	v_lshl_add_u64 v[110:111], v[108:109], 0, s[14:15]
; #define MODW_LD(W, j0) do { _Pragma("unroll") for (int q = 0; q < 4; ++q) W[q] = *(const GAS f32x4*)(wp + (size_t)(((j0) + q) & 63) * 16 * 6144); } while (0)
; #define MODW_USE(W, j0) do { _Pragma("unroll") for (int q = 0; q < 4; ++q) { const int k = kg + 16 * ((j0) + q); _Pragma("unroll") for (int r = 0; r < 17; ++r) acc[r] += W[q] * sc[r * 1024 + k]; asm volatile("" ::: "memory"); } } while (0)
; __device__ __forceinline__ void p0_prologue(const Frame& F0) {
;     ...
;                 MODW_LD(wa, 0);
; #pragma unroll 1
;                 for (int j = 0; j < 64; j += 8) { MODW_LD(wb, j + 4); MODW_USE(wa, j); MODW_LD(wa, j + 8); MODW_USE(wb, j + 4); }
.LBB0_13:
	v_add_co_u32_e32 v90, vcc, s33, v110
	s_add_i32 s3, s2, 16
	s_nop 0
	v_addc_co_u32_e32 v91, vcc, -1, v111, vcc
	v_add_co_u32_e32 v92, vcc, s34, v110
	global_load_dwordx4 v[86:89], v[110:111], off nt
	s_nop 0
	v_addc_co_u32_e32 v93, vcc, -1, v111, vcc
	v_add_co_u32_e32 v122, vcc, s35, v110
	ds_read2st64_b32 v[112:113], v131 offset1:16
	ds_read2st64_b32 v[114:115], v131 offset0:32 offset1:48
	ds_read2st64_b32 v[116:117], v131 offset0:64 offset1:80
	ds_read2st64_b32 v[118:119], v131 offset0:96 offset1:112
	ds_read2st64_b32 v[120:121], v131 offset0:128 offset1:144
	ds_read2st64_b32 v[124:125], v131 offset0:160 offset1:176
	ds_read2st64_b32 v[126:127], v131 offset0:192 offset1:208
	ds_read2st64_b32 v[128:129], v131 offset0:224 offset1:240
	v_add_u32_e32 v135, 0x10000, v131
	s_and_b32 s3, s3, 56
	v_addc_co_u32_e32 v123, vcc, -1, v111, vcc
	v_add_u32_e32 v132, 64, v131
	v_add_u32_e32 v136, 0x10040, v131
	global_load_dwordx4 v[98:101], v[90:91], off nt
	global_load_dwordx4 v[94:97], v[92:93], off nt
	s_nop 0
	global_load_dwordx4 v[90:93], v[122:123], off nt
	ds_read_b32 v122, v135
	s_mul_i32 s12, s3, 0x60000
	v_add_u32_e32 v133, 0x80, v131
	ds_read2st64_b32 v[142:143], v132 offset1:16
	ds_read2st64_b32 v[144:145], v132 offset0:32 offset1:48
	ds_read2st64_b32 v[146:147], v132 offset0:64 offset1:80
	ds_read2st64_b32 v[148:149], v132 offset0:96 offset1:112
	ds_read2st64_b32 v[150:151], v132 offset0:128 offset1:144
	ds_read2st64_b32 v[152:153], v132 offset0:160 offset1:176
	ds_read2st64_b32 v[154:155], v132 offset0:192 offset1:208
	ds_read2st64_b32 v[156:157], v132 offset0:224 offset1:240
	ds_read_b32 v136, v136
	v_lshl_add_u64 v[176:177], v[108:109], 0, s[12:13]
	v_add_u32_e32 v137, 0x10080, v131
	v_add_u32_e32 v134, 0xc0, v131
	v_add_u32_e32 v138, 0x100c0, v131
	ds_read2st64_b32 v[158:159], v133 offset1:16
	ds_read2st64_b32 v[160:161], v133 offset0:32 offset1:48
	ds_read2st64_b32 v[162:163], v133 offset0:64 offset1:80
	ds_read2st64_b32 v[164:165], v133 offset0:96 offset1:112
	ds_read2st64_b32 v[166:167], v133 offset0:128 offset1:144
	ds_read2st64_b32 v[168:169], v133 offset0:160 offset1:176
	ds_read2st64_b32 v[170:171], v133 offset0:192 offset1:208
	ds_read2st64_b32 v[172:173], v133 offset0:224 offset1:240
	ds_read_b32 v174, v137
	v_add_co_u32_e32 v194, vcc, s29, v176
	ds_read2st64_b32 v[178:179], v134 offset1:16
	ds_read2st64_b32 v[180:181], v134 offset0:32 offset1:48
	ds_read2st64_b32 v[182:183], v134 offset0:64 offset1:80
	ds_read2st64_b32 v[184:185], v134 offset0:96 offset1:112
	ds_read2st64_b32 v[186:187], v134 offset0:128 offset1:144
	ds_read2st64_b32 v[188:189], v134 offset0:160 offset1:176
	ds_read2st64_b32 v[190:191], v134 offset0:192 offset1:208
	ds_read2st64_b32 v[192:193], v134 offset0:224 offset1:240
	ds_read_b32 v138, v138
	v_addc_co_u32_e32 v195, vcc, 0, v177, vcc
	v_add_co_u32_e32 v196, vcc, s30, v176
	s_waitcnt vmcnt(4) lgkmcnt(14)
	v_pk_fma_f32 v[84:85], v[40:41], v[112:113], v[84:85] op_sel_hi:[1,0,1]
	v_pk_fma_f32 v[82:83], v[38:39], v[112:113], v[82:83] op_sel_hi:[1,0,1]
	v_mov_b32_e32 v112, v113
	v_pk_fma_f32 v[80:81], v[40:41], v[114:115], v[80:81] op_sel_hi:[1,0,1]
	v_pk_fma_f32 v[78:79], v[38:39], v[114:115], v[78:79] op_sel_hi:[1,0,1]
	v_mov_b32_e32 v114, v115
	v_pk_fma_f32 v[76:77], v[40:41], v[116:117], v[76:77] op_sel_hi:[1,0,1]
	v_pk_fma_f32 v[74:75], v[38:39], v[116:117], v[74:75] op_sel_hi:[1,0,1]
	v_mov_b32_e32 v116, v117
	v_pk_fma_f32 v[72:73], v[40:41], v[118:119], v[72:73] op_sel_hi:[1,0,1]
	v_pk_fma_f32 v[70:71], v[38:39], v[118:119], v[70:71] op_sel_hi:[1,0,1]
	v_mov_b32_e32 v118, v119
	v_pk_fma_f32 v[68:69], v[40:41], v[120:121], v[68:69] op_sel_hi:[1,0,1]
	v_pk_fma_f32 v[66:67], v[38:39], v[120:121], v[66:67] op_sel_hi:[1,0,1]
	v_mov_b32_e32 v120, v121
	v_pk_fma_f32 v[32:33], v[40:41], v[124:125], v[32:33] op_sel_hi:[1,0,1]
	v_pk_fma_f32 v[30:31], v[38:39], v[124:125], v[30:31] op_sel_hi:[1,0,1]
	v_mov_b32_e32 v124, v125
	v_pk_fma_f32 v[28:29], v[40:41], v[126:127], v[28:29] op_sel_hi:[1,0,1]
	v_pk_fma_f32 v[26:27], v[38:39], v[126:127], v[26:27] op_sel_hi:[1,0,1]
	v_mov_b32_e32 v126, v127
	v_pk_fma_f32 v[24:25], v[40:41], v[128:129], v[24:25] op_sel_hi:[1,0,1]
	v_pk_fma_f32 v[22:23], v[38:39], v[128:129], v[22:23] op_sel_hi:[1,0,1]
	v_mov_b32_e32 v128, v129
	v_addc_co_u32_e32 v197, vcc, 0, v177, vcc
	v_pk_fma_f32 v[64:65], v[40:41], v[112:113], v[64:65] op_sel_hi:[1,0,1]
	v_pk_fma_f32 v[62:63], v[38:39], v[112:113], v[62:63] op_sel_hi:[1,0,1]
	v_pk_fma_f32 v[60:61], v[40:41], v[114:115], v[60:61] op_sel_hi:[1,0,1]
	v_pk_fma_f32 v[58:59], v[38:39], v[114:115], v[58:59] op_sel_hi:[1,0,1]
	v_pk_fma_f32 v[56:57], v[40:41], v[116:117], v[56:57] op_sel_hi:[1,0,1]
	v_pk_fma_f32 v[54:55], v[38:39], v[116:117], v[54:55] op_sel_hi:[1,0,1]
	v_pk_fma_f32 v[52:53], v[40:41], v[118:119], v[52:53] op_sel_hi:[1,0,1]
	v_pk_fma_f32 v[50:51], v[38:39], v[118:119], v[50:51] op_sel_hi:[1,0,1]
	v_pk_fma_f32 v[20:21], v[40:41], v[120:121], v[20:21] op_sel_hi:[1,0,1]
	v_pk_fma_f32 v[18:19], v[38:39], v[120:121], v[18:19] op_sel_hi:[1,0,1]
	v_pk_fma_f32 v[16:17], v[40:41], v[124:125], v[16:17] op_sel_hi:[1,0,1]
	v_pk_fma_f32 v[14:15], v[38:39], v[124:125], v[14:15] op_sel_hi:[1,0,1]
	v_pk_fma_f32 v[12:13], v[40:41], v[126:127], v[12:13] op_sel_hi:[1,0,1]
	v_pk_fma_f32 v[10:11], v[38:39], v[126:127], v[10:11] op_sel_hi:[1,0,1]
	v_pk_fma_f32 v[8:9], v[40:41], v[128:129], v[8:9] op_sel_hi:[1,0,1]
	v_pk_fma_f32 v[6:7], v[38:39], v[128:129], v[6:7] op_sel_hi:[1,0,1]
	v_pk_fma_f32 v[4:5], v[40:41], v[122:123], v[4:5] op_sel_hi:[1,0,1]
	v_pk_fma_f32 v[2:3], v[38:39], v[122:123], v[2:3] op_sel_hi:[1,0,1]
	v_mov_b32_e32 v112, v143
	v_mov_b32_e32 v114, v145
	v_mov_b32_e32 v116, v147
	v_mov_b32_e32 v118, v149
	v_mov_b32_e32 v120, v151
	v_mov_b32_e32 v122, v153
	v_mov_b32_e32 v124, v155
	v_mov_b32_e32 v126, v157
	v_add_co_u32_e32 v198, vcc, s31, v176
	v_pk_fma_f32 v[84:85], v[48:49], v[142:143], v[84:85] op_sel_hi:[1,0,1]
	v_pk_fma_f32 v[82:83], v[46:47], v[142:143], v[82:83] op_sel_hi:[1,0,1]
	v_pk_fma_f32 v[80:81], v[48:49], v[144:145], v[80:81] op_sel_hi:[1,0,1]
	v_pk_fma_f32 v[78:79], v[46:47], v[144:145], v[78:79] op_sel_hi:[1,0,1]
	v_pk_fma_f32 v[76:77], v[48:49], v[146:147], v[76:77] op_sel_hi:[1,0,1]
	v_pk_fma_f32 v[74:75], v[46:47], v[146:147], v[74:75] op_sel_hi:[1,0,1]
	v_pk_fma_f32 v[72:73], v[48:49], v[148:149], v[72:73] op_sel_hi:[1,0,1]
	v_pk_fma_f32 v[70:71], v[46:47], v[148:149], v[70:71] op_sel_hi:[1,0,1]
	v_pk_fma_f32 v[68:69], v[48:49], v[150:151], v[68:69] op_sel_hi:[1,0,1]
	v_pk_fma_f32 v[66:67], v[46:47], v[150:151], v[66:67] op_sel_hi:[1,0,1]
	v_pk_fma_f32 v[32:33], v[48:49], v[152:153], v[32:33] op_sel_hi:[1,0,1]
	v_pk_fma_f32 v[30:31], v[46:47], v[152:153], v[30:31] op_sel_hi:[1,0,1]
	v_pk_fma_f32 v[28:29], v[48:49], v[154:155], v[28:29] op_sel_hi:[1,0,1]
	v_pk_fma_f32 v[26:27], v[46:47], v[154:155], v[26:27] op_sel_hi:[1,0,1]
	v_pk_fma_f32 v[24:25], v[48:49], v[156:157], v[24:25] op_sel_hi:[1,0,1]
	v_pk_fma_f32 v[22:23], v[46:47], v[156:157], v[22:23] op_sel_hi:[1,0,1]
	v_pk_fma_f32 v[4:5], v[48:49], v[136:137], v[4:5] op_sel_hi:[1,0,1]
	v_pk_fma_f32 v[2:3], v[46:47], v[136:137], v[2:3] op_sel_hi:[1,0,1]
	v_pk_fma_f32 v[64:65], v[48:49], v[112:113], v[64:65] op_sel_hi:[1,0,1]
	v_pk_fma_f32 v[62:63], v[46:47], v[112:113], v[62:63] op_sel_hi:[1,0,1]
	v_pk_fma_f32 v[60:61], v[48:49], v[114:115], v[60:61] op_sel_hi:[1,0,1]
	v_pk_fma_f32 v[58:59], v[46:47], v[114:115], v[58:59] op_sel_hi:[1,0,1]
	v_pk_fma_f32 v[56:57], v[48:49], v[116:117], v[56:57] op_sel_hi:[1,0,1]
	v_pk_fma_f32 v[54:55], v[46:47], v[116:117], v[54:55] op_sel_hi:[1,0,1]
	v_pk_fma_f32 v[52:53], v[48:49], v[118:119], v[52:53] op_sel_hi:[1,0,1]
	v_pk_fma_f32 v[50:51], v[46:47], v[118:119], v[50:51] op_sel_hi:[1,0,1]
	v_pk_fma_f32 v[20:21], v[48:49], v[120:121], v[20:21] op_sel_hi:[1,0,1]
	v_pk_fma_f32 v[18:19], v[46:47], v[120:121], v[18:19] op_sel_hi:[1,0,1]
	v_pk_fma_f32 v[16:17], v[48:49], v[122:123], v[16:17] op_sel_hi:[1,0,1]
	v_pk_fma_f32 v[14:15], v[46:47], v[122:123], v[14:15] op_sel_hi:[1,0,1]
	v_pk_fma_f32 v[12:13], v[48:49], v[124:125], v[12:13] op_sel_hi:[1,0,1]
	v_pk_fma_f32 v[10:11], v[46:47], v[124:125], v[10:11] op_sel_hi:[1,0,1]
	v_pk_fma_f32 v[8:9], v[48:49], v[126:127], v[8:9] op_sel_hi:[1,0,1]
	v_pk_fma_f32 v[6:7], v[46:47], v[126:127], v[6:7] op_sel_hi:[1,0,1]
	v_mov_b32_e32 v112, v159
	v_mov_b32_e32 v114, v161
	v_mov_b32_e32 v116, v163
	v_mov_b32_e32 v118, v165
	s_waitcnt lgkmcnt(13)
	v_mov_b32_e32 v120, v167
	s_waitcnt lgkmcnt(12)
	v_mov_b32_e32 v122, v169
	s_waitcnt lgkmcnt(11)
	v_mov_b32_e32 v124, v171
	s_waitcnt lgkmcnt(10)
	v_mov_b32_e32 v126, v173
	v_add_u32_e32 v140, 0x10100, v131
	v_add_u32_e32 v139, 0x10140, v131
	v_addc_co_u32_e32 v199, vcc, 0, v177, vcc
	v_pk_fma_f32 v[84:85], v[44:45], v[158:159], v[84:85] op_sel_hi:[1,0,1]
	v_pk_fma_f32 v[82:83], v[42:43], v[158:159], v[82:83] op_sel_hi:[1,0,1]
	v_pk_fma_f32 v[80:81], v[44:45], v[160:161], v[80:81] op_sel_hi:[1,0,1]
	v_pk_fma_f32 v[78:79], v[42:43], v[160:161], v[78:79] op_sel_hi:[1,0,1]
	v_pk_fma_f32 v[76:77], v[44:45], v[162:163], v[76:77] op_sel_hi:[1,0,1]
	v_pk_fma_f32 v[74:75], v[42:43], v[162:163], v[74:75] op_sel_hi:[1,0,1]
	v_pk_fma_f32 v[72:73], v[44:45], v[164:165], v[72:73] op_sel_hi:[1,0,1]
	v_pk_fma_f32 v[70:71], v[42:43], v[164:165], v[70:71] op_sel_hi:[1,0,1]
	v_pk_fma_f32 v[68:69], v[44:45], v[166:167], v[68:69] op_sel_hi:[1,0,1]
	v_pk_fma_f32 v[66:67], v[42:43], v[166:167], v[66:67] op_sel_hi:[1,0,1]
	v_pk_fma_f32 v[32:33], v[44:45], v[168:169], v[32:33] op_sel_hi:[1,0,1]
	v_pk_fma_f32 v[30:31], v[42:43], v[168:169], v[30:31] op_sel_hi:[1,0,1]
	v_pk_fma_f32 v[28:29], v[44:45], v[170:171], v[28:29] op_sel_hi:[1,0,1]
	v_pk_fma_f32 v[26:27], v[42:43], v[170:171], v[26:27] op_sel_hi:[1,0,1]
	v_pk_fma_f32 v[24:25], v[44:45], v[172:173], v[24:25] op_sel_hi:[1,0,1]
	v_pk_fma_f32 v[22:23], v[42:43], v[172:173], v[22:23] op_sel_hi:[1,0,1]
	s_waitcnt lgkmcnt(9)
	v_pk_fma_f32 v[4:5], v[44:45], v[174:175], v[4:5] op_sel_hi:[1,0,1]
	v_pk_fma_f32 v[2:3], v[42:43], v[174:175], v[2:3] op_sel_hi:[1,0,1]
	v_pk_fma_f32 v[64:65], v[44:45], v[112:113], v[64:65] op_sel_hi:[1,0,1]
	v_pk_fma_f32 v[62:63], v[42:43], v[112:113], v[62:63] op_sel_hi:[1,0,1]
	v_pk_fma_f32 v[60:61], v[44:45], v[114:115], v[60:61] op_sel_hi:[1,0,1]
	v_pk_fma_f32 v[58:59], v[42:43], v[114:115], v[58:59] op_sel_hi:[1,0,1]
	v_pk_fma_f32 v[56:57], v[44:45], v[116:117], v[56:57] op_sel_hi:[1,0,1]
	v_pk_fma_f32 v[54:55], v[42:43], v[116:117], v[54:55] op_sel_hi:[1,0,1]
	v_pk_fma_f32 v[52:53], v[44:45], v[118:119], v[52:53] op_sel_hi:[1,0,1]
	v_pk_fma_f32 v[50:51], v[42:43], v[118:119], v[50:51] op_sel_hi:[1,0,1]
	v_pk_fma_f32 v[20:21], v[44:45], v[120:121], v[20:21] op_sel_hi:[1,0,1]
	v_pk_fma_f32 v[18:19], v[42:43], v[120:121], v[18:19] op_sel_hi:[1,0,1]
	v_pk_fma_f32 v[16:17], v[44:45], v[122:123], v[16:17] op_sel_hi:[1,0,1]
	v_pk_fma_f32 v[14:15], v[42:43], v[122:123], v[14:15] op_sel_hi:[1,0,1]
	v_pk_fma_f32 v[12:13], v[44:45], v[124:125], v[12:13] op_sel_hi:[1,0,1]
	v_pk_fma_f32 v[10:11], v[42:43], v[124:125], v[10:11] op_sel_hi:[1,0,1]
	v_pk_fma_f32 v[8:9], v[44:45], v[126:127], v[8:9] op_sel_hi:[1,0,1]
	v_pk_fma_f32 v[6:7], v[42:43], v[126:127], v[6:7] op_sel_hi:[1,0,1]
	s_waitcnt lgkmcnt(8)
	v_mov_b32_e32 v112, v179
	s_waitcnt lgkmcnt(7)
; #define MODW_LD(W, j0) do { _Pragma("unroll") for (int q = 0; q < 4; ++q) W[q] = *(const GAS f32x4*)(wp + (size_t)(((j0) + q) & 63) * 16 * 6144); } while (0)
; #define MODW_USE(W, j0) do { _Pragma("unroll") for (int q = 0; q < 4; ++q) { const int k = kg + 16 * ((j0) + q); _Pragma("unroll") for (int r = 0; r < 17; ++r) acc[r] += W[q] * sc[r * 1024 + k]; asm volatile("" ::: "memory"); } } while (0)
; __device__ __forceinline__ void p0_prologue(const Frame& F0) {
;     ...
;                 MODW_LD(wa, 0);
; #pragma unroll 1
;                 for (int j = 0; j < 64; j += 8) { MODW_LD(wb, j + 4); MODW_USE(wa, j); MODW_LD(wa, j + 8); MODW_USE(wb, j + 4); }
	v_mov_b32_e32 v114, v181
	s_waitcnt lgkmcnt(6)
	v_mov_b32_e32 v116, v183
	s_waitcnt lgkmcnt(5)
	v_mov_b32_e32 v118, v185
	s_waitcnt lgkmcnt(4)
	v_mov_b32_e32 v120, v187
	s_waitcnt lgkmcnt(3)
	v_mov_b32_e32 v122, v189
	s_waitcnt lgkmcnt(2)
	v_mov_b32_e32 v124, v191
	s_waitcnt lgkmcnt(1)
	v_mov_b32_e32 v126, v193
	ds_read2st64_b32 v[200:201], v131 offset0:1 offset1:17
	ds_read2st64_b32 v[202:203], v131 offset0:33 offset1:49
	ds_read2st64_b32 v[204:205], v131 offset0:65 offset1:81
	ds_read2st64_b32 v[206:207], v131 offset0:97 offset1:113
	ds_read2st64_b32 v[208:209], v131 offset0:129 offset1:145
	ds_read2st64_b32 v[210:211], v131 offset0:161 offset1:177
	ds_read2st64_b32 v[212:213], v131 offset0:193 offset1:209
	ds_read2st64_b32 v[214:215], v131 offset0:225 offset1:241
	ds_read_b32 v140, v140
	global_load_dwordx4 v[38:41], v[176:177], off nt
	global_load_dwordx4 v[46:49], v[194:195], off nt
	v_pk_fma_f32 v[84:85], v[36:37], v[178:179], v[84:85] op_sel_hi:[1,0,1]
	v_pk_fma_f32 v[82:83], v[34:35], v[178:179], v[82:83] op_sel_hi:[1,0,1]
	v_pk_fma_f32 v[80:81], v[36:37], v[180:181], v[80:81] op_sel_hi:[1,0,1]
	v_pk_fma_f32 v[78:79], v[34:35], v[180:181], v[78:79] op_sel_hi:[1,0,1]
	v_pk_fma_f32 v[76:77], v[36:37], v[182:183], v[76:77] op_sel_hi:[1,0,1]
	v_pk_fma_f32 v[74:75], v[34:35], v[182:183], v[74:75] op_sel_hi:[1,0,1]
	v_pk_fma_f32 v[72:73], v[36:37], v[184:185], v[72:73] op_sel_hi:[1,0,1]
	v_pk_fma_f32 v[70:71], v[34:35], v[184:185], v[70:71] op_sel_hi:[1,0,1]
	v_pk_fma_f32 v[68:69], v[36:37], v[186:187], v[68:69] op_sel_hi:[1,0,1]
	v_pk_fma_f32 v[66:67], v[34:35], v[186:187], v[66:67] op_sel_hi:[1,0,1]
	v_pk_fma_f32 v[32:33], v[36:37], v[188:189], v[32:33] op_sel_hi:[1,0,1]
	v_pk_fma_f32 v[30:31], v[34:35], v[188:189], v[30:31] op_sel_hi:[1,0,1]
	v_pk_fma_f32 v[28:29], v[36:37], v[190:191], v[28:29] op_sel_hi:[1,0,1]
	v_pk_fma_f32 v[26:27], v[34:35], v[190:191], v[26:27] op_sel_hi:[1,0,1]
	v_pk_fma_f32 v[24:25], v[36:37], v[192:193], v[24:25] op_sel_hi:[1,0,1]
	v_pk_fma_f32 v[22:23], v[34:35], v[192:193], v[22:23] op_sel_hi:[1,0,1]
	s_waitcnt lgkmcnt(9)
	v_pk_fma_f32 v[4:5], v[36:37], v[138:139], v[4:5] op_sel_hi:[1,0,1]
	v_pk_fma_f32 v[2:3], v[34:35], v[138:139], v[2:3] op_sel_hi:[1,0,1]
	global_load_dwordx4 v[42:45], v[196:197], off nt
	v_pk_fma_f32 v[64:65], v[36:37], v[112:113], v[64:65] op_sel_hi:[1,0,1]
	v_pk_fma_f32 v[62:63], v[34:35], v[112:113], v[62:63] op_sel_hi:[1,0,1]
	v_pk_fma_f32 v[60:61], v[36:37], v[114:115], v[60:61] op_sel_hi:[1,0,1]
	v_pk_fma_f32 v[58:59], v[34:35], v[114:115], v[58:59] op_sel_hi:[1,0,1]
	v_pk_fma_f32 v[56:57], v[36:37], v[116:117], v[56:57] op_sel_hi:[1,0,1]
	v_pk_fma_f32 v[54:55], v[34:35], v[116:117], v[54:55] op_sel_hi:[1,0,1]
	v_pk_fma_f32 v[52:53], v[36:37], v[118:119], v[52:53] op_sel_hi:[1,0,1]
	v_pk_fma_f32 v[50:51], v[34:35], v[118:119], v[50:51] op_sel_hi:[1,0,1]
	v_pk_fma_f32 v[20:21], v[36:37], v[120:121], v[20:21] op_sel_hi:[1,0,1]
	v_pk_fma_f32 v[18:19], v[34:35], v[120:121], v[18:19] op_sel_hi:[1,0,1]
	v_pk_fma_f32 v[16:17], v[36:37], v[122:123], v[16:17] op_sel_hi:[1,0,1]
	v_pk_fma_f32 v[14:15], v[34:35], v[122:123], v[14:15] op_sel_hi:[1,0,1]
	v_pk_fma_f32 v[12:13], v[36:37], v[124:125], v[12:13] op_sel_hi:[1,0,1]
	v_pk_fma_f32 v[10:11], v[34:35], v[124:125], v[10:11] op_sel_hi:[1,0,1]
	v_pk_fma_f32 v[8:9], v[36:37], v[126:127], v[8:9] op_sel_hi:[1,0,1]
	v_pk_fma_f32 v[6:7], v[34:35], v[126:127], v[6:7] op_sel_hi:[1,0,1]
	global_load_dwordx4 v[34:37], v[198:199], off nt
	ds_read2st64_b32 v[128:129], v132 offset0:1 offset1:17
	ds_read2st64_b32 v[136:137], v132 offset0:33 offset1:49
	ds_read2st64_b32 v[142:143], v132 offset0:65 offset1:81
	ds_read2st64_b32 v[144:145], v132 offset0:97 offset1:113
	ds_read2st64_b32 v[146:147], v132 offset0:129 offset1:145
	ds_read2st64_b32 v[148:149], v132 offset0:161 offset1:177
	ds_read2st64_b32 v[150:151], v132 offset0:193 offset1:209
	ds_read2st64_b32 v[152:153], v132 offset0:225 offset1:241
	ds_read_b32 v132, v139
	v_add_u32_e32 v141, 0x10180, v131
	ds_read2st64_b32 v[138:139], v133 offset0:1 offset1:17
	ds_read2st64_b32 v[154:155], v133 offset0:33 offset1:49
	ds_read2st64_b32 v[156:157], v133 offset0:65 offset1:81
	ds_read2st64_b32 v[158:159], v133 offset0:97 offset1:113
	ds_read2st64_b32 v[160:161], v133 offset0:129 offset1:145
	ds_read2st64_b32 v[162:163], v133 offset0:161 offset1:177
	ds_read2st64_b32 v[164:165], v133 offset0:193 offset1:209
	ds_read2st64_b32 v[166:167], v133 offset0:225 offset1:241
	ds_read_b32 v168, v141
	v_add_u32_e32 v216, 0x101c0, v131
	ds_read2st64_b32 v[170:171], v134 offset0:1 offset1:17
	ds_read2st64_b32 v[172:173], v134 offset0:33 offset1:49
	ds_read2st64_b32 v[174:175], v134 offset0:65 offset1:81
	ds_read2st64_b32 v[176:177], v134 offset0:97 offset1:113
	ds_read2st64_b32 v[178:179], v134 offset0:129 offset1:145
	ds_read2st64_b32 v[180:181], v134 offset0:161 offset1:177
	ds_read2st64_b32 v[182:183], v134 offset0:193 offset1:209
	ds_read2st64_b32 v[134:135], v134 offset0:225 offset1:241
	ds_read_b32 v184, v216
	s_waitcnt lgkmcnt(14)
	v_mov_b32_e32 v112, v201
	v_mov_b32_e32 v114, v203
	v_mov_b32_e32 v116, v205
	v_mov_b32_e32 v118, v207
	v_mov_b32_e32 v120, v209
	v_mov_b32_e32 v122, v211
	v_mov_b32_e32 v124, v213
	v_mov_b32_e32 v126, v215
	v_mov_b32_e32 v186, v129
	v_mov_b32_e32 v188, v137
	v_mov_b32_e32 v190, v143
	v_mov_b32_e32 v192, v145
	v_mov_b32_e32 v194, v147
	v_mov_b32_e32 v196, v149
	v_mov_b32_e32 v198, v151
	v_mov_b32_e32 v216, v153
	s_waitcnt vmcnt(6)
	v_pk_fma_f32 v[84:85], v[100:101], v[200:201], v[84:85] op_sel_hi:[1,0,1]
	v_pk_fma_f32 v[82:83], v[98:99], v[200:201], v[82:83] op_sel_hi:[1,0,1]
	v_pk_fma_f32 v[64:65], v[100:101], v[112:113], v[64:65] op_sel_hi:[1,0,1]
	v_pk_fma_f32 v[62:63], v[98:99], v[112:113], v[62:63] op_sel_hi:[1,0,1]
	v_pk_fma_f32 v[80:81], v[100:101], v[202:203], v[80:81] op_sel_hi:[1,0,1]
	v_pk_fma_f32 v[78:79], v[98:99], v[202:203], v[78:79] op_sel_hi:[1,0,1]
	v_pk_fma_f32 v[60:61], v[100:101], v[114:115], v[60:61] op_sel_hi:[1,0,1]
	v_pk_fma_f32 v[58:59], v[98:99], v[114:115], v[58:59] op_sel_hi:[1,0,1]
	v_pk_fma_f32 v[76:77], v[100:101], v[204:205], v[76:77] op_sel_hi:[1,0,1]
	v_pk_fma_f32 v[74:75], v[98:99], v[204:205], v[74:75] op_sel_hi:[1,0,1]
	v_pk_fma_f32 v[56:57], v[100:101], v[116:117], v[56:57] op_sel_hi:[1,0,1]
	v_pk_fma_f32 v[54:55], v[98:99], v[116:117], v[54:55] op_sel_hi:[1,0,1]
	v_pk_fma_f32 v[72:73], v[100:101], v[206:207], v[72:73] op_sel_hi:[1,0,1]
	v_pk_fma_f32 v[70:71], v[98:99], v[206:207], v[70:71] op_sel_hi:[1,0,1]
	v_pk_fma_f32 v[52:53], v[100:101], v[118:119], v[52:53] op_sel_hi:[1,0,1]
	v_pk_fma_f32 v[50:51], v[98:99], v[118:119], v[50:51] op_sel_hi:[1,0,1]
	v_pk_fma_f32 v[68:69], v[100:101], v[208:209], v[68:69] op_sel_hi:[1,0,1]
	v_pk_fma_f32 v[66:67], v[98:99], v[208:209], v[66:67] op_sel_hi:[1,0,1]
	v_pk_fma_f32 v[20:21], v[100:101], v[120:121], v[20:21] op_sel_hi:[1,0,1]
	v_pk_fma_f32 v[18:19], v[98:99], v[120:121], v[18:19] op_sel_hi:[1,0,1]
	v_pk_fma_f32 v[32:33], v[100:101], v[210:211], v[32:33] op_sel_hi:[1,0,1]
	v_pk_fma_f32 v[30:31], v[98:99], v[210:211], v[30:31] op_sel_hi:[1,0,1]
	v_pk_fma_f32 v[16:17], v[100:101], v[122:123], v[16:17] op_sel_hi:[1,0,1]
	v_pk_fma_f32 v[14:15], v[98:99], v[122:123], v[14:15] op_sel_hi:[1,0,1]
	v_pk_fma_f32 v[28:29], v[100:101], v[212:213], v[28:29] op_sel_hi:[1,0,1]
	v_pk_fma_f32 v[26:27], v[98:99], v[212:213], v[26:27] op_sel_hi:[1,0,1]
	v_pk_fma_f32 v[12:13], v[100:101], v[124:125], v[12:13] op_sel_hi:[1,0,1]
	v_pk_fma_f32 v[10:11], v[98:99], v[124:125], v[10:11] op_sel_hi:[1,0,1]
	v_pk_fma_f32 v[24:25], v[100:101], v[214:215], v[24:25] op_sel_hi:[1,0,1]
	v_pk_fma_f32 v[22:23], v[98:99], v[214:215], v[22:23] op_sel_hi:[1,0,1]
	v_pk_fma_f32 v[8:9], v[100:101], v[126:127], v[8:9] op_sel_hi:[1,0,1]
	v_pk_fma_f32 v[6:7], v[98:99], v[126:127], v[6:7] op_sel_hi:[1,0,1]
	v_pk_fma_f32 v[4:5], v[100:101], v[140:141], v[4:5] op_sel_hi:[1,0,1]
	v_pk_fma_f32 v[2:3], v[98:99], v[140:141], v[2:3] op_sel_hi:[1,0,1]
	v_mov_b32_e32 v218, v139
	v_mov_b32_e32 v220, v155
	v_mov_b32_e32 v222, v157
	v_mov_b32_e32 v224, v159
	s_waitcnt lgkmcnt(13)
	v_mov_b32_e32 v226, v161
	s_waitcnt lgkmcnt(12)
	v_mov_b32_e32 v228, v163
	s_waitcnt lgkmcnt(11)
	v_mov_b32_e32 v230, v165
	s_waitcnt lgkmcnt(10)
	v_mov_b32_e32 v232, v167
	s_waitcnt vmcnt(5)
	v_pk_fma_f32 v[84:85], v[96:97], v[128:129], v[84:85] op_sel_hi:[1,0,1]
	v_pk_fma_f32 v[82:83], v[94:95], v[128:129], v[82:83] op_sel_hi:[1,0,1]
	v_pk_fma_f32 v[64:65], v[96:97], v[186:187], v[64:65] op_sel_hi:[1,0,1]
	v_pk_fma_f32 v[62:63], v[94:95], v[186:187], v[62:63] op_sel_hi:[1,0,1]
	v_pk_fma_f32 v[80:81], v[96:97], v[136:137], v[80:81] op_sel_hi:[1,0,1]
	v_pk_fma_f32 v[78:79], v[94:95], v[136:137], v[78:79] op_sel_hi:[1,0,1]
	v_pk_fma_f32 v[60:61], v[96:97], v[188:189], v[60:61] op_sel_hi:[1,0,1]
	v_pk_fma_f32 v[58:59], v[94:95], v[188:189], v[58:59] op_sel_hi:[1,0,1]
	v_pk_fma_f32 v[76:77], v[96:97], v[142:143], v[76:77] op_sel_hi:[1,0,1]
	v_pk_fma_f32 v[74:75], v[94:95], v[142:143], v[74:75] op_sel_hi:[1,0,1]
	v_pk_fma_f32 v[56:57], v[96:97], v[190:191], v[56:57] op_sel_hi:[1,0,1]
	v_pk_fma_f32 v[54:55], v[94:95], v[190:191], v[54:55] op_sel_hi:[1,0,1]
	v_pk_fma_f32 v[72:73], v[96:97], v[144:145], v[72:73] op_sel_hi:[1,0,1]
	v_pk_fma_f32 v[70:71], v[94:95], v[144:145], v[70:71] op_sel_hi:[1,0,1]
	v_pk_fma_f32 v[52:53], v[96:97], v[192:193], v[52:53] op_sel_hi:[1,0,1]
	v_pk_fma_f32 v[50:51], v[94:95], v[192:193], v[50:51] op_sel_hi:[1,0,1]
	v_pk_fma_f32 v[68:69], v[96:97], v[146:147], v[68:69] op_sel_hi:[1,0,1]
	v_pk_fma_f32 v[66:67], v[94:95], v[146:147], v[66:67] op_sel_hi:[1,0,1]
	v_pk_fma_f32 v[20:21], v[96:97], v[194:195], v[20:21] op_sel_hi:[1,0,1]
	v_pk_fma_f32 v[18:19], v[94:95], v[194:195], v[18:19] op_sel_hi:[1,0,1]
	v_pk_fma_f32 v[32:33], v[96:97], v[148:149], v[32:33] op_sel_hi:[1,0,1]
	v_pk_fma_f32 v[30:31], v[94:95], v[148:149], v[30:31] op_sel_hi:[1,0,1]
	v_pk_fma_f32 v[16:17], v[96:97], v[196:197], v[16:17] op_sel_hi:[1,0,1]
	v_pk_fma_f32 v[14:15], v[94:95], v[196:197], v[14:15] op_sel_hi:[1,0,1]
	v_pk_fma_f32 v[28:29], v[96:97], v[150:151], v[28:29] op_sel_hi:[1,0,1]
	v_pk_fma_f32 v[26:27], v[94:95], v[150:151], v[26:27] op_sel_hi:[1,0,1]
	v_pk_fma_f32 v[12:13], v[96:97], v[198:199], v[12:13] op_sel_hi:[1,0,1]
	v_pk_fma_f32 v[10:11], v[94:95], v[198:199], v[10:11] op_sel_hi:[1,0,1]
	v_pk_fma_f32 v[24:25], v[96:97], v[152:153], v[24:25] op_sel_hi:[1,0,1]
	v_pk_fma_f32 v[22:23], v[94:95], v[152:153], v[22:23] op_sel_hi:[1,0,1]
	v_pk_fma_f32 v[8:9], v[96:97], v[216:217], v[8:9] op_sel_hi:[1,0,1]
	v_pk_fma_f32 v[6:7], v[94:95], v[216:217], v[6:7] op_sel_hi:[1,0,1]
	v_pk_fma_f32 v[4:5], v[96:97], v[132:133], v[4:5] op_sel_hi:[1,0,1]
	v_pk_fma_f32 v[2:3], v[94:95], v[132:133], v[2:3] op_sel_hi:[1,0,1]
	s_add_i32 s2, s2, 8
	s_waitcnt lgkmcnt(8)
	v_mov_b32_e32 v234, v171
	s_waitcnt lgkmcnt(7)
; #define MODW_LD(W, j0) do { _Pragma("unroll") for (int q = 0; q < 4; ++q) W[q] = *(const GAS f32x4*)(wp + (size_t)(((j0) + q) & 63) * 16 * 6144); } while (0)
; #define MODW_USE(W, j0) do { _Pragma("unroll") for (int q = 0; q < 4; ++q) { const int k = kg + 16 * ((j0) + q); _Pragma("unroll") for (int r = 0; r < 17; ++r) acc[r] += W[q] * sc[r * 1024 + k]; asm volatile("" ::: "memory"); } } while (0)
; __device__ __forceinline__ void p0_prologue(const Frame& F0) {
;     ...
;                 MODW_LD(wa, 0);
; #pragma unroll 1
;                 for (int j = 0; j < 64; j += 8) { MODW_LD(wb, j + 4); MODW_USE(wa, j); MODW_LD(wa, j + 8); MODW_USE(wb, j + 4); }
	v_mov_b32_e32 v236, v173
	s_waitcnt lgkmcnt(6)
	v_mov_b32_e32 v238, v175
	s_waitcnt lgkmcnt(5)
	v_mov_b32_e32 v240, v177
	s_waitcnt lgkmcnt(4)
	v_mov_b32_e32 v242, v179
	s_waitcnt lgkmcnt(3)
	v_mov_b32_e32 v244, v181
	s_waitcnt lgkmcnt(2)
	v_mov_b32_e32 v246, v183
	s_waitcnt lgkmcnt(1)
	v_mov_b32_e32 v248, v135
	s_waitcnt vmcnt(4)
	v_pk_fma_f32 v[84:85], v[92:93], v[138:139], v[84:85] op_sel_hi:[1,0,1]
	v_pk_fma_f32 v[82:83], v[90:91], v[138:139], v[82:83] op_sel_hi:[1,0,1]
	v_pk_fma_f32 v[64:65], v[92:93], v[218:219], v[64:65] op_sel_hi:[1,0,1]
	v_pk_fma_f32 v[62:63], v[90:91], v[218:219], v[62:63] op_sel_hi:[1,0,1]
	v_pk_fma_f32 v[80:81], v[92:93], v[154:155], v[80:81] op_sel_hi:[1,0,1]
	v_pk_fma_f32 v[78:79], v[90:91], v[154:155], v[78:79] op_sel_hi:[1,0,1]
	v_pk_fma_f32 v[60:61], v[92:93], v[220:221], v[60:61] op_sel_hi:[1,0,1]
	v_pk_fma_f32 v[58:59], v[90:91], v[220:221], v[58:59] op_sel_hi:[1,0,1]
	v_pk_fma_f32 v[76:77], v[92:93], v[156:157], v[76:77] op_sel_hi:[1,0,1]
	v_pk_fma_f32 v[74:75], v[90:91], v[156:157], v[74:75] op_sel_hi:[1,0,1]
	v_pk_fma_f32 v[56:57], v[92:93], v[222:223], v[56:57] op_sel_hi:[1,0,1]
	v_pk_fma_f32 v[54:55], v[90:91], v[222:223], v[54:55] op_sel_hi:[1,0,1]
	v_pk_fma_f32 v[72:73], v[92:93], v[158:159], v[72:73] op_sel_hi:[1,0,1]
	v_pk_fma_f32 v[70:71], v[90:91], v[158:159], v[70:71] op_sel_hi:[1,0,1]
	v_pk_fma_f32 v[52:53], v[92:93], v[224:225], v[52:53] op_sel_hi:[1,0,1]
	v_pk_fma_f32 v[50:51], v[90:91], v[224:225], v[50:51] op_sel_hi:[1,0,1]
	v_pk_fma_f32 v[68:69], v[92:93], v[160:161], v[68:69] op_sel_hi:[1,0,1]
	v_pk_fma_f32 v[66:67], v[90:91], v[160:161], v[66:67] op_sel_hi:[1,0,1]
	v_pk_fma_f32 v[20:21], v[92:93], v[226:227], v[20:21] op_sel_hi:[1,0,1]
	v_pk_fma_f32 v[18:19], v[90:91], v[226:227], v[18:19] op_sel_hi:[1,0,1]
	v_pk_fma_f32 v[32:33], v[92:93], v[162:163], v[32:33] op_sel_hi:[1,0,1]
	v_pk_fma_f32 v[30:31], v[90:91], v[162:163], v[30:31] op_sel_hi:[1,0,1]
	v_pk_fma_f32 v[16:17], v[92:93], v[228:229], v[16:17] op_sel_hi:[1,0,1]
	v_pk_fma_f32 v[14:15], v[90:91], v[228:229], v[14:15] op_sel_hi:[1,0,1]
	v_pk_fma_f32 v[28:29], v[92:93], v[164:165], v[28:29] op_sel_hi:[1,0,1]
	v_pk_fma_f32 v[26:27], v[90:91], v[164:165], v[26:27] op_sel_hi:[1,0,1]
	v_pk_fma_f32 v[12:13], v[92:93], v[230:231], v[12:13] op_sel_hi:[1,0,1]
	v_pk_fma_f32 v[10:11], v[90:91], v[230:231], v[10:11] op_sel_hi:[1,0,1]
	v_pk_fma_f32 v[24:25], v[92:93], v[166:167], v[24:25] op_sel_hi:[1,0,1]
	v_pk_fma_f32 v[22:23], v[90:91], v[166:167], v[22:23] op_sel_hi:[1,0,1]
	v_pk_fma_f32 v[8:9], v[92:93], v[232:233], v[8:9] op_sel_hi:[1,0,1]
	v_pk_fma_f32 v[6:7], v[90:91], v[232:233], v[6:7] op_sel_hi:[1,0,1]
	v_pk_fma_f32 v[4:5], v[92:93], v[168:169], v[4:5] op_sel_hi:[1,0,1]
	v_pk_fma_f32 v[2:3], v[90:91], v[168:169], v[2:3] op_sel_hi:[1,0,1]
	v_lshl_add_u64 v[110:111], v[110:111], 0, s[16:17]
	s_cmp_lt_u32 s2, 56
	v_add_u32_e32 v131, 0x200, v131
	v_pk_fma_f32 v[84:85], v[88:89], v[170:171], v[84:85] op_sel_hi:[1,0,1]
	v_pk_fma_f32 v[82:83], v[86:87], v[170:171], v[82:83] op_sel_hi:[1,0,1]
	v_pk_fma_f32 v[64:65], v[88:89], v[234:235], v[64:65] op_sel_hi:[1,0,1]
	v_pk_fma_f32 v[62:63], v[86:87], v[234:235], v[62:63] op_sel_hi:[1,0,1]
	v_pk_fma_f32 v[80:81], v[88:89], v[172:173], v[80:81] op_sel_hi:[1,0,1]
	v_pk_fma_f32 v[78:79], v[86:87], v[172:173], v[78:79] op_sel_hi:[1,0,1]
	v_pk_fma_f32 v[60:61], v[88:89], v[236:237], v[60:61] op_sel_hi:[1,0,1]
	v_pk_fma_f32 v[58:59], v[86:87], v[236:237], v[58:59] op_sel_hi:[1,0,1]
	v_pk_fma_f32 v[76:77], v[88:89], v[174:175], v[76:77] op_sel_hi:[1,0,1]
	v_pk_fma_f32 v[74:75], v[86:87], v[174:175], v[74:75] op_sel_hi:[1,0,1]
	v_pk_fma_f32 v[56:57], v[88:89], v[238:239], v[56:57] op_sel_hi:[1,0,1]
	v_pk_fma_f32 v[54:55], v[86:87], v[238:239], v[54:55] op_sel_hi:[1,0,1]
	v_pk_fma_f32 v[72:73], v[88:89], v[176:177], v[72:73] op_sel_hi:[1,0,1]
	v_pk_fma_f32 v[70:71], v[86:87], v[176:177], v[70:71] op_sel_hi:[1,0,1]
	v_pk_fma_f32 v[52:53], v[88:89], v[240:241], v[52:53] op_sel_hi:[1,0,1]
	v_pk_fma_f32 v[50:51], v[86:87], v[240:241], v[50:51] op_sel_hi:[1,0,1]
	v_pk_fma_f32 v[68:69], v[88:89], v[178:179], v[68:69] op_sel_hi:[1,0,1]
	v_pk_fma_f32 v[66:67], v[86:87], v[178:179], v[66:67] op_sel_hi:[1,0,1]
	v_pk_fma_f32 v[20:21], v[88:89], v[242:243], v[20:21] op_sel_hi:[1,0,1]
	v_pk_fma_f32 v[18:19], v[86:87], v[242:243], v[18:19] op_sel_hi:[1,0,1]
	v_pk_fma_f32 v[32:33], v[88:89], v[180:181], v[32:33] op_sel_hi:[1,0,1]
	v_pk_fma_f32 v[30:31], v[86:87], v[180:181], v[30:31] op_sel_hi:[1,0,1]
	v_pk_fma_f32 v[16:17], v[88:89], v[244:245], v[16:17] op_sel_hi:[1,0,1]
	v_pk_fma_f32 v[14:15], v[86:87], v[244:245], v[14:15] op_sel_hi:[1,0,1]
	v_pk_fma_f32 v[28:29], v[88:89], v[182:183], v[28:29] op_sel_hi:[1,0,1]
	v_pk_fma_f32 v[26:27], v[86:87], v[182:183], v[26:27] op_sel_hi:[1,0,1]
	v_pk_fma_f32 v[12:13], v[88:89], v[246:247], v[12:13] op_sel_hi:[1,0,1]
	v_pk_fma_f32 v[10:11], v[86:87], v[246:247], v[10:11] op_sel_hi:[1,0,1]
	v_pk_fma_f32 v[24:25], v[88:89], v[134:135], v[24:25] op_sel_hi:[1,0,1]
	v_pk_fma_f32 v[22:23], v[86:87], v[134:135], v[22:23] op_sel_hi:[1,0,1]
	v_pk_fma_f32 v[8:9], v[88:89], v[248:249], v[8:9] op_sel_hi:[1,0,1]
	v_pk_fma_f32 v[6:7], v[86:87], v[248:249], v[6:7] op_sel_hi:[1,0,1]
	s_waitcnt lgkmcnt(0)
	v_pk_fma_f32 v[4:5], v[88:89], v[184:185], v[4:5] op_sel_hi:[1,0,1]
	v_pk_fma_f32 v[2:3], v[86:87], v[184:185], v[2:3] op_sel_hi:[1,0,1]
	s_cbranch_scc1 .LBB0_13

; #define N1_XLD(X, r) do { const GAS f32x4* xin_ = (const GAS f32x4*)N1_XIN(r) + F.lane; _Pragma("unroll") for (int j = 0; j < 4; ++j) X[j] = xin_[64 * j]; } while (0)
; __device__ __forceinline__ void n1_phase(const Frame& F0, int L, int nrows) {
;     ...
;         f32x4 X0[4], X1[4], X2[4];
;         N1_XLD(X0, rbeg); N1_XLD(X1, rbeg + 1);
.LBB0_369:
	s_lshl_b64 s[2:3], s[2:3], 12
	s_add_u32 s0, s0, s2
	s_addc_u32 s1, s1, s3
	s_waitcnt vmcnt(12)
	v_lshlrev_b32_e32 v84, 4, v1
	global_load_dwordx4 v[62:65], v84, s[0:1] nt
	global_load_dwordx4 v[58:61], v84, s[0:1] offset:1024 nt
	global_load_dwordx4 v[54:57], v84, s[0:1] offset:2048 nt
	global_load_dwordx4 v[46:49], v84, s[0:1] offset:3072 nt
	s_cmpk_gt_i32 s38, 0x7ffe
	s_mov_b64 s[4:5], -1
	s_cbranch_scc0 .LBB0_371
	v_readlane_b32 s0, v255, 1
	s_add_i32 s12, s38, 0xffff8001
	s_mov_b64 s[4:5], 0
	v_mov_b32_e32 v2, s0
	ds_read_b64 v[2:3], v2
	s_mov_b64 s[2:3], s[12:13]
	s_waitcnt lgkmcnt(0)
	v_readfirstlane_b32 s0, v2
	v_readfirstlane_b32 s1, v3

; #define N1_XLD(X, r) do { const GAS f32x4* xin_ = (const GAS f32x4*)N1_XIN(r) + F.lane; _Pragma("unroll") for (int j = 0; j < 4; ++j) X[j] = xin_[64 * j]; } while (0)
; __device__ __forceinline__ void n1_phase(const Frame& F0, int L, int nrows) {
;     ...
;         N1_XLD(X0, rbeg); N1_XLD(X1, rbeg + 1);
.LBB0_373:
	s_lshl_b64 s[2:3], s[2:3], 12
	s_add_u32 s0, s0, s2
	s_addc_u32 s1, s1, s3
	s_nop 1
	global_load_dwordx4 v[14:17], v84, s[0:1] nt
	global_load_dwordx4 v[10:13], v84, s[0:1] offset:1024 nt
	global_load_dwordx4 v[6:9], v84, s[0:1] offset:2048 nt
	global_load_dwordx4 v[2:5], v84, s[0:1] offset:3072 nt
	v_readlane_b32 s4, v255, 22
	s_cmp_lt_i32 s4, 3
	v_lshlrev_b32_e32 v190, 2, v1
	v_lshlrev_b32_e32 v82, 3, v1
	s_cbranch_scc1 .LBB0_395
	v_readlane_b32 s0, v252, 20
	v_mov_b32_e32 v83, v191
	v_readlane_b32 s1, v252, 21
	s_ashr_i32 s39, s38, 31
	v_mov_b32_e32 v85, v191
	v_lshl_add_u64 v[94:95], s[0:1], 0, v[82:83]
	s_lshl_b64 s[0:1], s[38:39], 10
	v_or_b32_e32 v98, s0, v190
	v_mov_b32_e32 v99, s1
	s_lshl_b64 s[0:1], s[38:39], 11
	s_mov_b32 s17, -1
	s_add_i32 s18, s4, -1
	s_mov_b32 s19, 4
	v_lshl_add_u64 v[86:87], s[28:29], 0, v[84:85]
	v_or_b32_e32 v88, 0x100, v190
	v_or_b32_e32 v90, 0x200, v190
	v_or_b32_e32 v92, 0x300, v190
	v_lshl_add_u64 v[96:97], s[96:97], 0, v[190:191]
	v_or_b32_e32 v100, s0, v82
	v_mov_b32_e32 v101, s1
.LBB0_375:
	s_add_i32 s8, s38, s19
	s_add_i32 s0, s8, -4
	s_min_i32 s0, s0, 0x8000
	s_ashr_i32 s0, s0, 11
	s_cmp_eq_u32 s0, s17
	v_lshlrev_b32_e32 v1, 2, v190
	v_lshlrev_b32_e32 v89, 2, v88
	v_lshlrev_b32_e32 v85, 2, v90
	v_lshlrev_b32_e32 v83, 2, v92
	s_cbranch_scc1 .LBB0_377
	s_mul_i32 s2, s0, 0x1800
	s_ashr_i32 s3, s2, 31
	s_lshl_b64 s[2:3], s[2:3], 2
	v_readlane_b32 s1, v255, 20
	s_add_u32 s2, s1, s2
	v_readlane_b32 s1, v255, 21
	s_addc_u32 s3, s1, s3
	s_add_u32 s4, s2, 0x1000
	s_addc_u32 s5, s3, 0
	global_load_dwordx4 v[34:37], v1, s[4:5]
	global_load_dwordx4 v[38:41], v89, s[4:5]
	global_load_dwordx4 v[42:45], v85, s[4:5]
	global_load_dwordx4 v[50:53], v83, s[4:5]
	s_waitcnt vmcnt(19)
	flat_load_dwordx4 v[66:69], v[86:87]
	flat_load_dwordx4 v[70:73], v[86:87] offset:1024
	flat_load_dwordx4 v[74:77], v[86:87] offset:2048
	flat_load_dwordx4 v[78:81], v[86:87] offset:3072
	global_load_dwordx4 v[26:29], v1, s[2:3] nt
	global_load_dwordx4 v[22:25], v1, s[2:3] offset:1024 nt
	global_load_dwordx4 v[18:21], v1, s[2:3] offset:2048 nt
	global_load_dwordx4 v[30:33], v1, s[2:3] offset:3072 nt
	s_mov_b32 s17, s0
	s_waitcnt vmcnt(0)
	v_pk_add_f32 v[36:37], v[36:37], 1.0 op_sel_hi:[1,0]
	v_pk_add_f32 v[34:35], v[34:35], 1.0 op_sel_hi:[1,0]
	v_pk_add_f32 v[40:41], v[40:41], 1.0 op_sel_hi:[1,0]
	v_pk_add_f32 v[38:39], v[38:39], 1.0 op_sel_hi:[1,0]
	v_pk_add_f32 v[102:103], v[44:45], 1.0 op_sel_hi:[1,0]
	v_pk_add_f32 v[104:105], v[42:43], 1.0 op_sel_hi:[1,0]
	v_pk_add_f32 v[106:107], v[52:53], 1.0 op_sel_hi:[1,0]
	v_pk_add_f32 v[108:109], v[50:51], 1.0 op_sel_hi:[1,0]
	s_waitcnt lgkmcnt(0)
	v_pk_mul_f32 v[52:53], v[68:69], v[36:37]
	v_pk_mul_f32 v[50:51], v[66:67], v[34:35]
	v_pk_mul_f32 v[44:45], v[72:73], v[40:41]
	v_pk_mul_f32 v[42:43], v[70:71], v[38:39]
	v_pk_mul_f32 v[40:41], v[76:77], v[102:103]
	v_pk_mul_f32 v[38:39], v[74:75], v[104:105]
	v_pk_mul_f32 v[36:37], v[80:81], v[106:107]
	v_pk_mul_f32 v[34:35], v[78:79], v[108:109]

; #define GAS __attribute__((address_space(1)))
; __device__ __forceinline__ bf16_t* x_row_ptr(Frame& F, int row) { return (bf16_t*)(F.ws + WS_X) + (size_t)row * D; }
; __device__ __forceinline__ void n1_finish(Frame& F, int L, int row, const f32x4 (&v)[4], const f32x4 (&gs)[4], const f32x4 (&sh)[4]) {
;     bf16_t* H = (bf16_t*)(F.ws + WS_H);
;     x_store_row(x_row_ptr(F, row), F.lane, v);
;     float ss = 0.f;
; #pragma unroll
;     for (int j = 0; j < 4; ++j) ss += (v[j][0] * v[j][0] + v[j][1] * v[j][1]) + (v[j][2] * v[j][2] + v[j][3] * v[j][3]);
;     const float rinv = __builtin_amdgcn_rsqf(wave_sum(ss) * (1.0f / D) + EPS);
;     if ((L & 1) == 0) {
;         GAS unsigned* o4 = (GAS unsigned*)((unsigned char*)H + (size_t)row * D) + F.lane;
; #pragma unroll
;         for (int j = 0; j < 4; ++j) { const f32x4 h = ((v[j] * rinv) * gs[j] + sh[j]) * pg8::SC_H2; o4[64 * j] = pg8::pack4_fp8(h[0], h[1], h[2], h[3]); }
.LBB0_381:
	s_waitcnt vmcnt(7)
	v_pk_mul_f32 v[66:67], v[64:65], v[64:65]
	v_pk_mul_f32 v[68:69], v[62:63], v[62:63]
	s_lshl_b64 s[4:5], s[4:5], 12
	v_pk_mov_b32 v[70:71], v[68:69], v[66:67] op_sel:[1,0]
	v_mov_b32_e32 v69, v67
	v_pk_add_f32 v[66:67], v[70:71], v[68:69]
	s_waitcnt vmcnt(6)
	v_pk_mul_f32 v[68:69], v[60:61], v[60:61]
	v_pk_add_f32 v[66:67], v[66:67], v[66:67] op_sel_hi:[0,1]
	v_pk_mul_f32 v[70:71], v[58:59], v[58:59]
	s_waitcnt vmcnt(5)
	v_mul_f32_e32 v66, v54, v54
	v_pk_mov_b32 v[72:73], v[70:71], v[68:69] op_sel:[1,0]
	v_mov_b32_e32 v71, v69
	v_pk_add_f32 v[68:69], v[72:73], v[70:71]
	v_pk_fma_f32 v[70:71], v[54:55], v[54:55], v[66:67] op_sel_hi:[1,1,0]
	v_mul_f32_e32 v66, v56, v56
	v_pk_add_f32 v[68:69], v[68:69], v[68:69] op_sel_hi:[0,1]
	v_pk_fma_f32 v[72:73], v[56:57], v[56:57], v[66:67] op_sel_hi:[1,1,0]
	s_waitcnt vmcnt(4)
	v_mul_f32_e32 v70, v46, v46
	v_mul_f32_e32 v72, v47, v47
	v_mul_f32_e32 v68, v48, v48
	v_mul_f32_e32 v66, v49, v49
	v_pk_add_f32 v[70:71], v[70:71], v[72:73]
	v_pk_add_f32 v[66:67], v[68:69], v[66:67]
	s_add_u32 s2, s2, s4
	v_pk_add_f32 v[66:67], v[70:71], v[66:67]
	s_addc_u32 s3, s3, s5
	v_add_f32_e32 v66, v66, v67
	v_and_b32_e32 v67, 64, v211
	v_add_u32_e32 v110, 64, v67
	v_xor_b32_e32 v67, 1, v211
	v_cmp_lt_i32_e32 vcc, v67, v110
	global_load_dwordx4 v[78:81], v84, s[2:3] nt
	global_load_dwordx4 v[74:77], v84, s[2:3] offset:1024 nt
	v_cndmask_b32_e32 v67, v211, v67, vcc
	v_lshlrev_b32_e32 v91, 2, v67
	ds_bpermute_b32 v67, v91, v66
	v_lshl_add_u64 v[104:105], s[82:83], 0, v[100:101]
	s_mov_b32 s1, 0x31b00000
	v_cvt_pk_bf16_f32 v107, v64, v65
	v_cvt_pk_bf16_f32 v106, v62, v63
	s_waitcnt lgkmcnt(0)
	v_add_f32_e32 v66, v66, v67
	v_xor_b32_e32 v67, 2, v211
	v_cmp_lt_i32_e32 vcc, v67, v110
	s_nop 1
	v_cndmask_b32_e32 v67, v211, v67, vcc
	v_lshlrev_b32_e32 v93, 2, v67
	ds_bpermute_b32 v67, v93, v66
	s_waitcnt lgkmcnt(0)
	v_add_f32_e32 v103, v66, v67
	v_xor_b32_e32 v66, 4, v211
	v_cmp_lt_i32_e32 vcc, v66, v110
	s_nop 1
	v_cndmask_b32_e32 v66, v211, v66, vcc
	v_lshlrev_b32_e32 v102, 2, v66
	global_load_dwordx4 v[70:73], v84, s[2:3] offset:2048 nt
	global_load_dwordx4 v[66:69], v84, s[2:3] offset:3072 nt
	ds_bpermute_b32 v108, v102, v103
	s_add_i32 s2, s8, -3
	s_waitcnt lgkmcnt(0)
	v_add_f32_e32 v111, v103, v108
	v_xor_b32_e32 v103, 8, v211
	v_cmp_lt_i32_e32 vcc, v103, v110
	s_nop 1
	v_cndmask_b32_e32 v103, v211, v103, vcc
	v_lshlrev_b32_e32 v103, 2, v103
	ds_bpermute_b32 v112, v103, v111
	v_add_co_u32_e32 v108, vcc, s1, v104
	v_xor_b32_e32 v104, 16, v211
	s_nop 0
	v_addc_co_u32_e32 v109, vcc, 0, v105, vcc
	v_cmp_lt_i32_e32 vcc, v104, v110
	s_waitcnt lgkmcnt(0)
	v_add_f32_e32 v105, v111, v112
	global_store_dwordx2 v[108:109], v[106:107], off
	v_cndmask_b32_e32 v104, v211, v104, vcc
	v_lshlrev_b32_e32 v104, 2, v104
	ds_bpermute_b32 v111, v104, v105
	v_cvt_pk_bf16_f32 v107, v60, v61
	v_cvt_pk_bf16_f32 v106, v58, v59
	global_store_dwordx2 v[108:109], v[106:107], off offset:512
	v_cvt_pk_bf16_f32 v107, v56, v57
	s_waitcnt lgkmcnt(0)
	v_add_f32_e32 v111, v105, v111
	v_xor_b32_e32 v105, 32, v211
	v_cmp_lt_i32_e32 vcc, v105, v110
	v_cvt_pk_bf16_f32 v106, v54, v55
	global_store_dwordx2 v[108:109], v[106:107], off offset:1024
	v_cvt_pk_bf16_f32 v106, v46, v47
	s_mov_b32 s1, 0x1b300000
	v_cndmask_b32_e32 v105, v211, v105, vcc
	v_lshlrev_b32_e32 v105, 2, v105
	ds_bpermute_b32 v110, v105, v111
	s_waitcnt lgkmcnt(0)
	v_add_f32_e32 v107, v111, v110
	v_fmamk_f32 v107, v107, 0x3a800000, v250
	v_rsq_f32_e32 v110, v107
	v_cvt_pk_bf16_f32 v107, v48, v49
	global_store_dwordx2 v[108:109], v[106:107], off offset:1536
	v_mov_b32_e32 v108, v191
	v_pk_mul_f32 v[62:63], v[62:63], v[110:111] op_sel_hi:[1,0]
	v_pk_mul_f32 v[64:65], v[64:65], v[110:111] op_sel_hi:[1,0]
	v_pk_fma_f32 v[62:63], v[50:51], v[62:63], v[26:27]
	v_pk_fma_f32 v[64:65], v[52:53], v[64:65], v[28:29]
	v_pk_mul_f32 v[62:63], v[62:63], s[16:17] op_sel_hi:[1,0]
	v_pk_mul_f32 v[58:59], v[58:59], v[110:111] op_sel_hi:[1,0]
	v_med3_f32 v62, v62, s15, v212
	v_med3_f32 v63, v63, s15, v212
	v_cvt_pk_fp8_f32 v108, v62, v63
	v_pk_mul_f32 v[62:63], v[64:65], s[16:17] op_sel_hi:[1,0]
	v_pk_fma_f32 v[58:59], v[42:43], v[58:59], v[22:23]
	v_med3_f32 v62, v62, s15, v212
	v_med3_f32 v63, v63, s15, v212
	v_pk_mul_f32 v[58:59], v[58:59], s[16:17] op_sel_hi:[1,0]
	v_cvt_pk_fp8_f32 v108, v62, v63 op_sel:[0,0,1]
	v_med3_f32 v58, v58, s15, v212
	v_med3_f32 v59, v59, s15, v212
	v_mov_b32_e32 v62, v191
	v_pk_mul_f32 v[60:61], v[60:61], v[110:111] op_sel_hi:[1,0]
	v_cvt_pk_fp8_f32 v62, v58, v59
	v_pk_fma_f32 v[60:61], v[44:45], v[60:61], v[24:25]
	v_pk_mul_f32 v[54:55], v[54:55], v[110:111] op_sel_hi:[1,0]
	v_pk_mul_f32 v[58:59], v[60:61], s[16:17] op_sel_hi:[1,0]
	v_pk_fma_f32 v[54:55], v[38:39], v[54:55], v[18:19]
	v_pk_mul_f32 v[46:47], v[46:47], v[110:111] op_sel_hi:[1,0]
	v_med3_f32 v58, v58, s15, v212
	v_med3_f32 v59, v59, s15, v212
	v_pk_mul_f32 v[56:57], v[56:57], v[110:111] op_sel_hi:[1,0]
	v_pk_mul_f32 v[54:55], v[54:55], s[16:17] op_sel_hi:[1,0]
	v_pk_fma_f32 v[46:47], v[34:35], v[46:47], v[30:31]
	v_cvt_pk_fp8_f32 v62, v58, v59 op_sel:[0,0,1]
	v_pk_fma_f32 v[56:57], v[40:41], v[56:57], v[20:21]
	v_med3_f32 v54, v54, s15, v212
	v_med3_f32 v55, v55, s15, v212
	v_mov_b32_e32 v58, v191
	v_pk_mul_f32 v[46:47], v[46:47], s[16:17] op_sel_hi:[1,0]
	v_cvt_pk_fp8_f32 v58, v54, v55
	v_pk_mul_f32 v[54:55], v[56:57], s[16:17] op_sel_hi:[1,0]
	v_med3_f32 v46, v46, s15, v212
	v_med3_f32 v47, v47, s15, v212
	v_mov_b32_e32 v56, v191
	v_pk_mul_f32 v[48:49], v[48:49], v[110:111] op_sel_hi:[1,0]
	v_cvt_pk_fp8_f32 v56, v46, v47
	v_pk_fma_f32 v[48:49], v[36:37], v[48:49], v[32:33]
	v_lshl_add_u64 v[106:107], s[82:83], 0, v[98:99]
	v_pk_mul_f32 v[46:47], v[48:49], s[16:17] op_sel_hi:[1,0]
	v_med3_f32 v54, v54, s15, v212
	v_med3_f32 v46, v46, s15, v212
	v_med3_f32 v47, v47, s15, v212
	v_med3_f32 v55, v55, s15, v212
	v_cvt_pk_fp8_f32 v56, v46, v47 op_sel:[0,0,1]
	v_cvt_pk_fp8_f32 v58, v54, v55 op_sel:[0,0,1]
	v_add_co_u32_e32 v54, vcc, s1, v106
	s_min_i32 s1, s2, 0x8000
	s_ashr_i32 s1, s1, 11
	v_addc_co_u32_e32 v55, vcc, 0, v107, vcc
	s_cmp_eq_u32 s1, s17
	global_store_dword v[54:55], v108, off
	global_store_dword v[54:55], v62, off offset:256
	global_store_dword v[54:55], v58, off offset:512
	global_store_dword v[54:55], v56, off offset:768
	s_cbranch_scc1 .LBB0_383
	s_mul_i32 s4, s1, 0x1800
	s_ashr_i32 s5, s4, 31
	s_lshl_b64 s[4:5], s[4:5], 2
	v_readlane_b32 s3, v255, 20
	s_add_u32 s4, s3, s4
	v_readlane_b32 s3, v255, 21
	s_addc_u32 s5, s3, s5
	s_add_u32 s6, s4, 0x1000
	s_addc_u32 s7, s5, 0
	global_load_dwordx4 v[34:37], v1, s[6:7]
	global_load_dwordx4 v[38:41], v89, s[6:7]
	global_load_dwordx4 v[42:45], v85, s[6:7]
	global_load_dwordx4 v[46:49], v83, s[6:7]
	flat_load_dwordx4 v[50:53], v[86:87]
	flat_load_dwordx4 v[54:57], v[86:87] offset:1024
	flat_load_dwordx4 v[58:61], v[86:87] offset:2048
	flat_load_dwordx4 v[62:65], v[86:87] offset:3072
	global_load_dwordx4 v[26:29], v1, s[4:5] nt
	global_load_dwordx4 v[22:25], v1, s[4:5] offset:1024 nt
	global_load_dwordx4 v[18:21], v1, s[4:5] offset:2048 nt
	global_load_dwordx4 v[30:33], v1, s[4:5] offset:3072 nt
	s_mov_b32 s17, s1
	s_waitcnt vmcnt(0)
	v_pk_add_f32 v[36:37], v[36:37], 1.0 op_sel_hi:[1,0]
	v_pk_add_f32 v[34:35], v[34:35], 1.0 op_sel_hi:[1,0]
	v_pk_add_f32 v[40:41], v[40:41], 1.0 op_sel_hi:[1,0]
	v_pk_add_f32 v[38:39], v[38:39], 1.0 op_sel_hi:[1,0]
	v_pk_add_f32 v[106:107], v[44:45], 1.0 op_sel_hi:[1,0]
	v_pk_add_f32 v[108:109], v[42:43], 1.0 op_sel_hi:[1,0]
	v_pk_add_f32 v[48:49], v[48:49], 1.0 op_sel_hi:[1,0]
	v_pk_add_f32 v[46:47], v[46:47], 1.0 op_sel_hi:[1,0]
	s_waitcnt lgkmcnt(0)
	v_pk_mul_f32 v[52:53], v[52:53], v[36:37]
	v_pk_mul_f32 v[50:51], v[50:51], v[34:35]
	v_pk_mul_f32 v[44:45], v[56:57], v[40:41]
	v_pk_mul_f32 v[42:43], v[54:55], v[38:39]
	v_pk_mul_f32 v[40:41], v[60:61], v[106:107]
	v_pk_mul_f32 v[38:39], v[58:59], v[108:109]
	v_pk_mul_f32 v[36:37], v[64:65], v[48:49]
	v_pk_mul_f32 v[34:35], v[62:63], v[46:47]

; #define GAS __attribute__((address_space(1)))
; __device__ __forceinline__ unsigned pk2(float lo, float hi) { unsigned r; asm("v_cvt_pk_bf16_f32 %0, %1, %2" : "=v"(r) : "v"(lo), "v"(hi)); return r; }
; __device__ __forceinline__ bf16_t* x_row_ptr(Frame& F, int row) { return (bf16_t*)(F.ws + WS_X) + (size_t)row * D; }
; #define N1_XLD(X, r) do { const GAS f32x4* xin_ = (const GAS f32x4*)N1_XIN(r) + F.lane; _Pragma("unroll") for (int j = 0; j < 4; ++j) X[j] = xin_[64 * j]; } while (0)
; #define N1_STEP0(XC, XI, kk) do { const int k_ = (kk), row_ = rbeg + k_; N1_MOD(row_); N1_XLD(XI, rbeg + (k_ + 2 < RPW ? k_ + 2 : RPW - 1)); n1_finish(F, L, row_, XC, gs, sh); } while (0)
; __device__ __forceinline__ void n1_finish(Frame& F, int L, int row, const f32x4 (&v)[4], const f32x4 (&gs)[4], const f32x4 (&sh)[4]) {
;     bf16_t* H = (bf16_t*)(F.ws + WS_H);
;     x_store_row(x_row_ptr(F, row), F.lane, v);
;     float ss = 0.f;
; #pragma unroll
;     for (int j = 0; j < 4; ++j) ss += (v[j][0] * v[j][0] + v[j][1] * v[j][1]) + (v[j][2] * v[j][2] + v[j][3] * v[j][3]);
;     const float rinv = __builtin_amdgcn_rsqf(wave_sum(ss) * (1.0f / D) + EPS);
;     if ((L & 1) == 0) {
;         GAS unsigned* o4 = (GAS unsigned*)((unsigned char*)H + (size_t)row * D) + F.lane;
; #pragma unroll
;         for (int j = 0; j < 4; ++j) { const f32x4 h = ((v[j] * rinv) * gs[j] + sh[j]) * pg8::SC_H2; o4[64 * j] = pg8::pack4_fp8(h[0], h[1], h[2], h[3]); }
;     } else {
;         GAS u32x2* o8 = (GAS u32x2*)(H + (size_t)row * D) + F.lane;
; #pragma unroll
;         for (int j = 0; j < 4; ++j) { const f32x4 h = (v[j] * rinv) * gs[j] + sh[j]; u32x2 w; w.x = pk2(h[0], h[1]); w.y = pk2(h[2], h[3]); o8[64 * j] = w; }
;     }
; }
; __device__ __forceinline__ void n1_phase(const Frame& F0, int L, int nrows) {
;     ...
;     if (L == 0) {
;     ...
;         f32x4 X0[4], X1[4], X2[4];
;         N1_XLD(X0, rbeg); N1_XLD(X1, rbeg + 1);
;         int k = 0;
;         for (; k + 2 < RPW; k += 3) { N1_STEP0(X0, X2, k); N1_STEP0(X1, X0, k + 1); N1_STEP0(X2, X1, k + 2); }
.LBB0_387:
	s_waitcnt vmcnt(15)
	v_pk_mul_f32 v[46:47], v[16:17], v[16:17]
	v_pk_mul_f32 v[48:49], v[14:15], v[14:15]
	s_lshl_b64 s[6:7], s[6:7], 12
	v_pk_mov_b32 v[54:55], v[48:49], v[46:47] op_sel:[1,0]
	v_mov_b32_e32 v49, v47
	v_pk_add_f32 v[46:47], v[54:55], v[48:49]
	s_waitcnt vmcnt(14)
	v_pk_mul_f32 v[48:49], v[12:13], v[12:13]
	v_pk_add_f32 v[46:47], v[46:47], v[46:47] op_sel_hi:[0,1]
	v_pk_mul_f32 v[54:55], v[10:11], v[10:11]
	s_waitcnt vmcnt(13)
	v_mul_f32_e32 v46, v6, v6
	v_pk_mov_b32 v[56:57], v[54:55], v[48:49] op_sel:[1,0]
	v_mov_b32_e32 v55, v49
	v_pk_add_f32 v[48:49], v[56:57], v[54:55]
	v_pk_fma_f32 v[54:55], v[6:7], v[6:7], v[46:47] op_sel_hi:[1,1,0]
	v_mul_f32_e32 v46, v8, v8
	v_pk_add_f32 v[48:49], v[48:49], v[48:49] op_sel_hi:[0,1]
	v_pk_fma_f32 v[56:57], v[8:9], v[8:9], v[46:47] op_sel_hi:[1,1,0]
	s_waitcnt vmcnt(12)
	v_mul_f32_e32 v54, v2, v2
	v_mul_f32_e32 v56, v3, v3
	v_mul_f32_e32 v48, v4, v4
	v_mul_f32_e32 v46, v5, v5
	v_pk_add_f32 v[54:55], v[54:55], v[56:57]
	v_pk_add_f32 v[46:47], v[48:49], v[46:47]
	s_add_u32 s4, s4, s6
	v_pk_add_f32 v[46:47], v[54:55], v[46:47]
	s_addc_u32 s5, s5, s7
	v_add_f32_e32 v46, v46, v47
	ds_bpermute_b32 v47, v91, v46
	s_ashr_i32 s3, s2, 31
	s_min_i32 s1, s0, 0x8000
	s_ashr_i32 s1, s1, 11
	s_waitcnt lgkmcnt(0)
	v_add_f32_e32 v46, v46, v47
	ds_bpermute_b32 v47, v93, v46
	s_waitcnt lgkmcnt(0)
	v_add_f32_e32 v106, v46, v47
	global_load_dwordx4 v[62:65], v84, s[4:5] nt
	global_load_dwordx4 v[58:61], v84, s[4:5] offset:1024 nt
	global_load_dwordx4 v[54:57], v84, s[4:5] offset:2048 nt
	global_load_dwordx4 v[46:49], v84, s[4:5] offset:3072 nt
	ds_bpermute_b32 v107, v102, v106
	s_lshl_b64 s[4:5], s[2:3], 11
	v_lshl_add_u64 v[108:109], v[94:95], 0, s[4:5]
	s_lshl_b64 s[2:3], s[2:3], 10
	s_cmp_eq_u32 s1, s17
	s_waitcnt lgkmcnt(0)
	v_add_f32_e32 v110, v106, v107
	ds_bpermute_b32 v111, v103, v110
	v_cvt_pk_bf16_f32 v107, v16, v17
	v_cvt_pk_bf16_f32 v106, v14, v15
	global_store_dwordx2 v[108:109], v[106:107], off
	v_cvt_pk_bf16_f32 v107, v12, v13
	s_waitcnt lgkmcnt(0)
	v_add_f32_e32 v110, v110, v111
	ds_bpermute_b32 v111, v104, v110
	v_cvt_pk_bf16_f32 v106, v10, v11
	global_store_dwordx2 v[108:109], v[106:107], off offset:512
	v_cvt_pk_bf16_f32 v107, v8, v9
	v_cvt_pk_bf16_f32 v106, v6, v7
	s_waitcnt lgkmcnt(0)
	v_add_f32_e32 v110, v110, v111
	ds_bpermute_b32 v111, v105, v110
	global_store_dwordx2 v[108:109], v[106:107], off offset:1024
	v_cvt_pk_bf16_f32 v106, v2, v3
	s_waitcnt lgkmcnt(0)
	v_add_f32_e32 v107, v110, v111
	v_fmamk_f32 v107, v107, 0x3a800000, v250
	v_rsq_f32_e32 v110, v107
	v_cvt_pk_bf16_f32 v107, v4, v5
	global_store_dwordx2 v[108:109], v[106:107], off offset:1536
	v_mov_b32_e32 v106, v191
	v_pk_mul_f32 v[14:15], v[14:15], v[110:111] op_sel_hi:[1,0]
	v_pk_mul_f32 v[16:17], v[16:17], v[110:111] op_sel_hi:[1,0]
	v_pk_fma_f32 v[14:15], v[50:51], v[14:15], v[26:27]
	v_pk_fma_f32 v[16:17], v[52:53], v[16:17], v[28:29]
	v_pk_mul_f32 v[14:15], v[14:15], s[16:17] op_sel_hi:[1,0]
	v_pk_mul_f32 v[10:11], v[10:11], v[110:111] op_sel_hi:[1,0]
	v_med3_f32 v14, v14, s15, v212
	v_med3_f32 v15, v15, s15, v212
	v_cvt_pk_fp8_f32 v106, v14, v15
	v_pk_mul_f32 v[14:15], v[16:17], s[16:17] op_sel_hi:[1,0]
	v_pk_fma_f32 v[10:11], v[42:43], v[10:11], v[22:23]
	v_med3_f32 v14, v14, s15, v212
	v_med3_f32 v15, v15, s15, v212
	v_pk_mul_f32 v[10:11], v[10:11], s[16:17] op_sel_hi:[1,0]
	v_cvt_pk_fp8_f32 v106, v14, v15 op_sel:[0,0,1]
	v_med3_f32 v10, v10, s15, v212
	v_med3_f32 v11, v11, s15, v212
	v_mov_b32_e32 v14, v191
	v_pk_mul_f32 v[12:13], v[12:13], v[110:111] op_sel_hi:[1,0]
	v_cvt_pk_fp8_f32 v14, v10, v11
	v_pk_fma_f32 v[12:13], v[44:45], v[12:13], v[24:25]
	v_pk_mul_f32 v[6:7], v[6:7], v[110:111] op_sel_hi:[1,0]
	v_pk_mul_f32 v[10:11], v[12:13], s[16:17] op_sel_hi:[1,0]
	v_pk_fma_f32 v[6:7], v[38:39], v[6:7], v[18:19]
	v_pk_mul_f32 v[2:3], v[2:3], v[110:111] op_sel_hi:[1,0]
	v_med3_f32 v10, v10, s15, v212
	v_med3_f32 v11, v11, s15, v212
	v_pk_mul_f32 v[8:9], v[8:9], v[110:111] op_sel_hi:[1,0]
	v_pk_mul_f32 v[6:7], v[6:7], s[16:17] op_sel_hi:[1,0]
	v_pk_fma_f32 v[2:3], v[34:35], v[2:3], v[30:31]
	v_cvt_pk_fp8_f32 v14, v10, v11 op_sel:[0,0,1]
	v_pk_fma_f32 v[8:9], v[40:41], v[8:9], v[20:21]
	v_med3_f32 v6, v6, s15, v212
	v_med3_f32 v7, v7, s15, v212
	v_mov_b32_e32 v10, v191
	v_pk_mul_f32 v[2:3], v[2:3], s[16:17] op_sel_hi:[1,0]
	v_cvt_pk_fp8_f32 v10, v6, v7
	v_pk_mul_f32 v[6:7], v[8:9], s[16:17] op_sel_hi:[1,0]
	v_med3_f32 v2, v2, s15, v212
	v_med3_f32 v3, v3, s15, v212
	v_mov_b32_e32 v8, v191
	v_pk_mul_f32 v[4:5], v[4:5], v[110:111] op_sel_hi:[1,0]
	v_cvt_pk_fp8_f32 v8, v2, v3
	v_pk_fma_f32 v[4:5], v[36:37], v[4:5], v[32:33]
	v_med3_f32 v6, v6, s15, v212
	v_pk_mul_f32 v[2:3], v[4:5], s[16:17] op_sel_hi:[1,0]
	v_med3_f32 v7, v7, s15, v212
	v_med3_f32 v2, v2, s15, v212
	v_med3_f32 v3, v3, s15, v212
	v_cvt_pk_fp8_f32 v8, v2, v3 op_sel:[0,0,1]
	v_cvt_pk_fp8_f32 v10, v6, v7 op_sel:[0,0,1]
	v_lshl_add_u64 v[6:7], v[96:97], 0, s[2:3]
	global_store_dword v[6:7], v106, off
	global_store_dword v[6:7], v14, off offset:256
	global_store_dword v[6:7], v10, off offset:512
	global_store_dword v[6:7], v8, off offset:768
	s_cbranch_scc1 .LBB0_389
	s_mul_i32 s2, s1, 0x1800
	s_ashr_i32 s3, s2, 31
	s_lshl_b64 s[2:3], s[2:3], 2
	v_readlane_b32 s4, v255, 20
	s_add_u32 s2, s4, s2
	v_readlane_b32 s4, v255, 21
	s_addc_u32 s3, s4, s3
	s_add_u32 s4, s2, 0x1000
	s_addc_u32 s5, s3, 0
	s_nop 1
	global_load_dwordx4 v[2:5], v1, s[4:5]
	global_load_dwordx4 v[6:9], v89, s[4:5]
	global_load_dwordx4 v[10:13], v85, s[4:5]
	global_load_dwordx4 v[14:17], v83, s[4:5]
	flat_load_dwordx4 v[34:37], v[86:87]
	flat_load_dwordx4 v[38:41], v[86:87] offset:1024
	flat_load_dwordx4 v[106:109], v[86:87] offset:2048
	flat_load_dwordx4 v[110:113], v[86:87] offset:3072
	global_load_dwordx4 v[26:29], v1, s[2:3] nt
	global_load_dwordx4 v[22:25], v1, s[2:3] offset:1024 nt
	global_load_dwordx4 v[18:21], v1, s[2:3] offset:2048 nt
	global_load_dwordx4 v[30:33], v1, s[2:3] offset:3072 nt
	s_mov_b32 s17, s1
	s_waitcnt vmcnt(0)
	v_pk_add_f32 v[4:5], v[4:5], 1.0 op_sel_hi:[1,0]
	v_pk_add_f32 v[2:3], v[2:3], 1.0 op_sel_hi:[1,0]
	v_pk_add_f32 v[8:9], v[8:9], 1.0 op_sel_hi:[1,0]
	v_pk_add_f32 v[6:7], v[6:7], 1.0 op_sel_hi:[1,0]
	v_pk_add_f32 v[12:13], v[12:13], 1.0 op_sel_hi:[1,0]
	v_pk_add_f32 v[10:11], v[10:11], 1.0 op_sel_hi:[1,0]
	v_pk_add_f32 v[16:17], v[16:17], 1.0 op_sel_hi:[1,0]
	v_pk_add_f32 v[14:15], v[14:15], 1.0 op_sel_hi:[1,0]
	s_waitcnt lgkmcnt(0)
	v_pk_mul_f32 v[52:53], v[36:37], v[4:5]
	v_pk_mul_f32 v[50:51], v[34:35], v[2:3]
	v_pk_mul_f32 v[44:45], v[40:41], v[8:9]
	v_pk_mul_f32 v[42:43], v[38:39], v[6:7]
	v_pk_mul_f32 v[40:41], v[108:109], v[12:13]
	v_pk_mul_f32 v[38:39], v[106:107], v[10:11]
	v_pk_mul_f32 v[36:37], v[112:113], v[16:17]
	v_pk_mul_f32 v[34:35], v[110:111], v[14:15]

; #define GAS __attribute__((address_space(1)))
; __device__ __forceinline__ unsigned pk2(float lo, float hi) { unsigned r; asm("v_cvt_pk_bf16_f32 %0, %1, %2" : "=v"(r) : "v"(lo), "v"(hi)); return r; }
; __device__ __forceinline__ bf16_t* x_row_ptr(Frame& F, int row) { return (bf16_t*)(F.ws + WS_X) + (size_t)row * D; }
; #define N1_XLD(X, r) do { const GAS f32x4* xin_ = (const GAS f32x4*)N1_XIN(r) + F.lane; _Pragma("unroll") for (int j = 0; j < 4; ++j) X[j] = xin_[64 * j]; } while (0)
; #define N1_STEP0(XC, XI, kk) do { const int k_ = (kk), row_ = rbeg + k_; N1_MOD(row_); N1_XLD(XI, rbeg + (k_ + 2 < RPW ? k_ + 2 : RPW - 1)); n1_finish(F, L, row_, XC, gs, sh); } while (0)
; __device__ __forceinline__ void n1_finish(Frame& F, int L, int row, const f32x4 (&v)[4], const f32x4 (&gs)[4], const f32x4 (&sh)[4]) {
;     bf16_t* H = (bf16_t*)(F.ws + WS_H);
;     x_store_row(x_row_ptr(F, row), F.lane, v);
;     float ss = 0.f;
; #pragma unroll
;     for (int j = 0; j < 4; ++j) ss += (v[j][0] * v[j][0] + v[j][1] * v[j][1]) + (v[j][2] * v[j][2] + v[j][3] * v[j][3]);
;     const float rinv = __builtin_amdgcn_rsqf(wave_sum(ss) * (1.0f / D) + EPS);
;     if ((L & 1) == 0) {
;         GAS unsigned* o4 = (GAS unsigned*)((unsigned char*)H + (size_t)row * D) + F.lane;
; #pragma unroll
;         for (int j = 0; j < 4; ++j) { const f32x4 h = ((v[j] * rinv) * gs[j] + sh[j]) * pg8::SC_H2; o4[64 * j] = pg8::pack4_fp8(h[0], h[1], h[2], h[3]); }
;     } else {
;         GAS u32x2* o8 = (GAS u32x2*)(H + (size_t)row * D) + F.lane;
; #pragma unroll
;         for (int j = 0; j < 4; ++j) { const f32x4 h = (v[j] * rinv) * gs[j] + sh[j]; u32x2 w; w.x = pk2(h[0], h[1]); w.y = pk2(h[2], h[3]); o8[64 * j] = w; }
;     }
; }
; __device__ __forceinline__ void n1_phase(const Frame& F0, int L, int nrows) {
;     ...
;         f32x4 X0[4], X1[4], X2[4];
;         N1_XLD(X0, rbeg); N1_XLD(X1, rbeg + 1);
;         int k = 0;
;         for (; k + 2 < RPW; k += 3) { N1_STEP0(X0, X2, k); N1_STEP0(X1, X0, k + 1); N1_STEP0(X2, X1, k + 2); }
.LBB0_393:
	s_waitcnt vmcnt(23)
	v_pk_mul_f32 v[2:3], v[80:81], v[80:81]
	v_pk_mul_f32 v[4:5], v[78:79], v[78:79]
	s_waitcnt vmcnt(20)
	v_mul_f32_e32 v1, v66, v66
	v_pk_mov_b32 v[6:7], v[4:5], v[2:3] op_sel:[1,0]
	v_mov_b32_e32 v5, v3
	v_pk_add_f32 v[2:3], v[6:7], v[4:5]
	v_pk_mul_f32 v[4:5], v[76:77], v[76:77]
	v_pk_mul_f32 v[6:7], v[74:75], v[74:75]
	v_pk_add_f32 v[2:3], v[2:3], v[2:3] op_sel:[0,1] op_sel_hi:[1,0]
	v_pk_mov_b32 v[8:9], v[6:7], v[4:5] op_sel:[1,0]
	v_mov_b32_e32 v7, v5
	v_pk_add_f32 v[4:5], v[8:9], v[6:7]
	v_mul_f32_e32 v6, v67, v67
	v_pk_add_f32 v[4:5], v[4:5], v[4:5] op_sel:[0,1] op_sel_hi:[1,0]
	v_mov_b32_e32 v3, v1
	v_mov_b32_e32 v5, v6
	v_pk_add_f32 v[2:3], v[2:3], v[4:5]
	v_mul_f32_e32 v4, v71, v71
	v_mul_f32_e32 v7, v68, v68
	v_pk_fma_f32 v[4:5], v[70:71], v[70:71], v[4:5] op_sel_hi:[1,1,0]
	v_mul_f32_e32 v6, v73, v73
	v_mul_f32_e32 v8, v69, v69
	v_mov_b32_e32 v5, v7
	v_pk_fma_f32 v[6:7], v[72:73], v[72:73], v[6:7] op_sel_hi:[1,1,0]
	s_lshl_b64 s[4:5], s[4:5], 12
	v_mov_b32_e32 v7, v8
	v_pk_add_f32 v[4:5], v[4:5], v[6:7]
	s_add_u32 s2, s2, s4
	v_pk_add_f32 v[2:3], v[2:3], v[4:5]
	s_addc_u32 s3, s3, s5
	v_add_f32_e32 v1, v2, v3
	ds_bpermute_b32 v2, v91, v1
	global_load_dwordx4 v[14:17], v84, s[2:3] nt
	global_load_dwordx4 v[10:13], v84, s[2:3] offset:1024 nt
	s_ashr_i32 s1, s0, 31
	v_readlane_b32 s4, v255, 22
	s_waitcnt lgkmcnt(0)
	v_add_f32_e32 v1, v1, v2
	ds_bpermute_b32 v2, v93, v1
	s_waitcnt lgkmcnt(0)
	v_add_f32_e32 v1, v1, v2
	global_load_dwordx4 v[6:9], v84, s[2:3] offset:2048 nt
	global_load_dwordx4 v[2:5], v84, s[2:3] offset:3072 nt
	ds_bpermute_b32 v83, v102, v1
	v_cvt_pk_bf16_f32 v102, v78, v79
	s_lshl_b64 s[2:3], s[0:1], 11
	v_lshl_add_u64 v[106:107], v[94:95], 0, s[2:3]
	s_lshl_b64 s[0:1], s[0:1], 10
	s_waitcnt lgkmcnt(0)
	v_add_f32_e32 v1, v1, v83
	ds_bpermute_b32 v83, v103, v1
	v_cvt_pk_bf16_f32 v103, v80, v81
	global_store_dwordx2 v[106:107], v[102:103], off
	v_cvt_pk_bf16_f32 v102, v74, v75
	v_cvt_pk_bf16_f32 v103, v76, v77
	s_waitcnt lgkmcnt(0)
	v_add_f32_e32 v1, v1, v83
	ds_bpermute_b32 v83, v104, v1
	global_store_dwordx2 v[106:107], v[102:103], off offset:512
	v_cvt_pk_bf16_f32 v102, v70, v71
	v_cvt_pk_bf16_f32 v103, v72, v73
	global_store_dwordx2 v[106:107], v[102:103], off offset:1024
	s_waitcnt lgkmcnt(0)
	v_add_f32_e32 v1, v1, v83
	ds_bpermute_b32 v83, v105, v1
	v_cvt_pk_bf16_f32 v102, v66, v67
	v_cvt_pk_bf16_f32 v103, v68, v69
	s_mov_b64 s[2:3], 0xc00
	global_store_dwordx2 v[106:107], v[102:103], off offset:1536
	s_waitcnt lgkmcnt(0)
	v_add_f32_e32 v1, v1, v83
	v_fmamk_f32 v1, v1, 0x3a800000, v250
	v_rsq_f32_e32 v104, v1
	v_mov_b32_e32 v83, v191
	v_lshl_add_u64 v[102:103], v[96:97], 0, s[0:1]
	s_add_i32 s0, s19, 3
	v_pk_mul_f32 v[78:79], v[78:79], v[104:105] op_sel_hi:[1,0]
	v_pk_mul_f32 v[80:81], v[80:81], v[104:105] op_sel_hi:[1,0]
	v_pk_fma_f32 v[78:79], v[50:51], v[78:79], v[26:27]
	v_pk_fma_f32 v[80:81], v[52:53], v[80:81], v[28:29]
	v_pk_mul_f32 v[78:79], v[78:79], s[16:17] op_sel_hi:[1,0]
	v_pk_mul_f32 v[74:75], v[74:75], v[104:105] op_sel_hi:[1,0]
	v_med3_f32 v1, v78, s15, v212
	v_med3_f32 v78, v79, s15, v212
	v_cvt_pk_fp8_f32 v83, v1, v78
	v_pk_mul_f32 v[78:79], v[80:81], s[16:17] op_sel_hi:[1,0]
	v_pk_fma_f32 v[74:75], v[42:43], v[74:75], v[22:23]
	v_med3_f32 v1, v78, s15, v212
	v_med3_f32 v78, v79, s15, v212
	v_pk_mul_f32 v[74:75], v[74:75], s[16:17] op_sel_hi:[1,0]
	v_cvt_pk_fp8_f32 v83, v1, v78 op_sel:[0,0,1]
	v_med3_f32 v1, v74, s15, v212
	v_med3_f32 v74, v75, s15, v212
	v_mov_b32_e32 v78, v191
	v_pk_mul_f32 v[76:77], v[76:77], v[104:105] op_sel_hi:[1,0]
	v_cvt_pk_fp8_f32 v78, v1, v74
	v_pk_fma_f32 v[76:77], v[44:45], v[76:77], v[24:25]
	v_pk_mul_f32 v[70:71], v[70:71], v[104:105] op_sel_hi:[1,0]
	v_pk_mul_f32 v[74:75], v[76:77], s[16:17] op_sel_hi:[1,0]
	v_pk_fma_f32 v[70:71], v[38:39], v[70:71], v[18:19]
	v_med3_f32 v1, v74, s15, v212
	v_med3_f32 v74, v75, s15, v212
	v_pk_mul_f32 v[70:71], v[70:71], s[16:17] op_sel_hi:[1,0]
	v_cvt_pk_fp8_f32 v78, v1, v74 op_sel:[0,0,1]
	v_med3_f32 v1, v70, s15, v212
	v_med3_f32 v70, v71, s15, v212
	v_mov_b32_e32 v74, v191
	v_pk_mul_f32 v[72:73], v[72:73], v[104:105] op_sel_hi:[1,0]
	v_cvt_pk_fp8_f32 v74, v1, v70
	v_pk_fma_f32 v[72:73], v[40:41], v[72:73], v[20:21]
	v_pk_mul_f32 v[66:67], v[66:67], v[104:105] op_sel_hi:[1,0]
	v_pk_mul_f32 v[70:71], v[72:73], s[16:17] op_sel_hi:[1,0]
	v_pk_fma_f32 v[66:67], v[34:35], v[66:67], v[30:31]
	v_med3_f32 v1, v70, s15, v212
	v_med3_f32 v70, v71, s15, v212
	v_pk_mul_f32 v[66:67], v[66:67], s[16:17] op_sel_hi:[1,0]
	v_cvt_pk_fp8_f32 v74, v1, v70 op_sel:[0,0,1]
	v_med3_f32 v1, v66, s15, v212
	v_med3_f32 v66, v67, s15, v212
	v_mov_b32_e32 v70, v191
	v_pk_mul_f32 v[68:69], v[68:69], v[104:105] op_sel_hi:[1,0]
	v_cvt_pk_fp8_f32 v70, v1, v66
	v_pk_fma_f32 v[68:69], v[36:37], v[68:69], v[32:33]
	s_add_i32 s1, s19, 1
	v_pk_mul_f32 v[66:67], v[68:69], s[16:17] op_sel_hi:[1,0]
	v_lshl_add_u64 v[98:99], v[98:99], 0, s[2:3]
	v_med3_f32 v1, v66, s15, v212
	v_med3_f32 v66, v67, s15, v212
	s_mov_b64 s[2:3], 0x1800
	v_cvt_pk_fp8_f32 v70, v1, v66 op_sel:[0,0,1]
	s_cmp_lt_i32 s1, s4
	v_lshl_add_u64 v[100:101], v[100:101], 0, s[2:3]
	global_store_dword v[102:103], v83, off
	global_store_dword v[102:103], v78, off offset:256
	global_store_dword v[102:103], v74, off offset:512
	global_store_dword v[102:103], v70, off offset:768
	s_cbranch_scc0 .LBB0_396
	s_mov_b32 s19, s0
	s_branch .LBB0_375

; #define GAS __attribute__((address_space(1)))
; __device__ __forceinline__ unsigned pk2(float lo, float hi) { unsigned r; asm("v_cvt_pk_bf16_f32 %0, %1, %2" : "=v"(r) : "v"(lo), "v"(hi)); return r; }
; __device__ __forceinline__ bf16_t* x_row_ptr(Frame& F, int row) { return (bf16_t*)(F.ws + WS_X) + (size_t)row * D; }
; __device__ __forceinline__ float wave_sum(float v) {
; #pragma unroll
;     for (int o = 1; o < 64; o <<= 1) v += __shfl_xor(v, o);
;     return v;
; }
; __device__ __forceinline__ void n1_finish(Frame& F, int L, int row, const f32x4 (&v)[4], const f32x4 (&gs)[4], const f32x4 (&sh)[4]) {
;     bf16_t* H = (bf16_t*)(F.ws + WS_H);
;     x_store_row(x_row_ptr(F, row), F.lane, v);
;     float ss = 0.f;
; #pragma unroll
;     for (int j = 0; j < 4; ++j) ss += (v[j][0] * v[j][0] + v[j][1] * v[j][1]) + (v[j][2] * v[j][2] + v[j][3] * v[j][3]);
;     const float rinv = __builtin_amdgcn_rsqf(wave_sum(ss) * (1.0f / D) + EPS);
;     if ((L & 1) == 0) {
;         GAS unsigned* o4 = (GAS unsigned*)((unsigned char*)H + (size_t)row * D) + F.lane;
; #pragma unroll
;         for (int j = 0; j < 4; ++j) { const f32x4 h = ((v[j] * rinv) * gs[j] + sh[j]) * pg8::SC_H2; o4[64 * j] = pg8::pack4_fp8(h[0], h[1], h[2], h[3]); }
;     } else {
;         GAS u32x2* o8 = (GAS u32x2*)(H + (size_t)row * D) + F.lane;
; #pragma unroll
;         for (int j = 0; j < 4; ++j) { const f32x4 h = (v[j] * rinv) * gs[j] + sh[j]; u32x2 w; w.x = pk2(h[0], h[1]); w.y = pk2(h[2], h[3]); o8[64 * j] = w; }
;     }
; }
.LBB0_396:
	s_cmp_ge_i32 s22, s4
	s_cbranch_scc1 .LBB0_403
	s_add_i32 s0, s22, s38
	s_min_i32 s1, s0, 0x8000
	s_ashr_i32 s1, s1, 11
	s_cmp_eq_u32 s1, s17
	s_cbranch_scc1 .LBB0_399
	s_mul_i32 s2, s1, 0x1800
	s_ashr_i32 s3, s2, 31
	s_lshl_b64 s[2:3], s[2:3], 2
	v_readlane_b32 s4, v255, 20
	s_add_u32 s2, s4, s2
	v_readlane_b32 s4, v255, 21
	s_addc_u32 s3, s4, s3
	s_add_u32 s4, s2, 0x1000
	s_addc_u32 s5, s3, 0
	v_or_b32_e32 v1, 0x400, v84
	v_mov_b32_e32 v85, v191
	global_load_dwordx4 v[34:37], v84, s[4:5]
	global_load_dwordx4 v[38:41], v1, s[4:5]
	v_or_b32_e32 v1, 0x800, v84
	global_load_dwordx4 v[42:45], v1, s[4:5]
	v_or_b32_e32 v1, 0xc00, v84
	global_load_dwordx4 v[50:53], v1, s[4:5]
	v_lshl_add_u64 v[18:19], s[28:29], 0, v[84:85]
	s_waitcnt vmcnt(19)
	flat_load_dwordx4 v[66:69], v[18:19]
	flat_load_dwordx4 v[70:73], v[18:19] offset:1024
	flat_load_dwordx4 v[74:77], v[18:19] offset:2048
	flat_load_dwordx4 v[78:81], v[18:19] offset:3072
	global_load_dwordx4 v[22:25], v84, s[2:3] offset:1024 nt
	s_nop 0
	global_load_dwordx4 v[18:21], v84, s[2:3] offset:2048 nt
	global_load_dwordx4 v[26:29], v84, s[2:3] nt
	global_load_dwordx4 v[30:33], v84, s[2:3] offset:3072 nt
	s_mov_b32 s17, s1
	s_waitcnt vmcnt(0)
	v_pk_add_f32 v[36:37], v[36:37], 1.0 op_sel_hi:[1,0]
	v_pk_add_f32 v[34:35], v[34:35], 1.0 op_sel_hi:[1,0]
	v_pk_add_f32 v[40:41], v[40:41], 1.0 op_sel_hi:[1,0]
	v_pk_add_f32 v[38:39], v[38:39], 1.0 op_sel_hi:[1,0]
	v_pk_add_f32 v[86:87], v[44:45], 1.0 op_sel_hi:[1,0]
	v_pk_add_f32 v[88:89], v[42:43], 1.0 op_sel_hi:[1,0]
	v_pk_add_f32 v[90:91], v[52:53], 1.0 op_sel_hi:[1,0]
	v_pk_add_f32 v[92:93], v[50:51], 1.0 op_sel_hi:[1,0]
	s_waitcnt lgkmcnt(0)
	v_pk_mul_f32 v[52:53], v[68:69], v[36:37]
	v_pk_mul_f32 v[50:51], v[66:67], v[34:35]
	v_pk_mul_f32 v[44:45], v[72:73], v[40:41]
	v_pk_mul_f32 v[42:43], v[70:71], v[38:39]
	v_pk_mul_f32 v[40:41], v[76:77], v[86:87]
	v_pk_mul_f32 v[38:39], v[74:75], v[88:89]
	v_pk_mul_f32 v[36:37], v[80:81], v[90:91]
	v_pk_mul_f32 v[34:35], v[78:79], v[92:93]
.LBB0_399:
	s_waitcnt vmcnt(7)
	v_pk_mul_f32 v[66:67], v[64:65], v[64:65]
	v_pk_mul_f32 v[68:69], v[62:63], v[62:63]
	v_and_b32_e32 v1, 64, v211
	v_pk_mov_b32 v[70:71], v[68:69], v[66:67] op_sel:[1,0]
	v_mov_b32_e32 v69, v67
	v_pk_add_f32 v[66:67], v[70:71], v[68:69]
	s_waitcnt vmcnt(6)
	v_pk_mul_f32 v[68:69], v[60:61], v[60:61]
	v_pk_add_f32 v[66:67], v[66:67], v[66:67] op_sel_hi:[0,1]
	v_pk_mul_f32 v[70:71], v[58:59], v[58:59]
	s_waitcnt vmcnt(5)
	v_mul_f32_e32 v66, v54, v54
	v_pk_mov_b32 v[72:73], v[70:71], v[68:69] op_sel:[1,0]
	v_mov_b32_e32 v71, v69
	v_pk_add_f32 v[68:69], v[72:73], v[70:71]
	v_pk_fma_f32 v[70:71], v[54:55], v[54:55], v[66:67] op_sel_hi:[1,1,0]
	v_mul_f32_e32 v66, v56, v56
	v_pk_fma_f32 v[72:73], v[56:57], v[56:57], v[66:67] op_sel_hi:[1,1,0]
	v_pk_add_f32 v[68:69], v[68:69], v[68:69] op_sel_hi:[0,1]
	s_waitcnt vmcnt(4)
	v_mul_f32_e32 v70, v46, v46
	v_mul_f32_e32 v72, v47, v47
	v_mul_f32_e32 v68, v48, v48
	v_mul_f32_e32 v66, v49, v49
	v_pk_add_f32 v[70:71], v[70:71], v[72:73]
	v_add_u32_e32 v72, 64, v1
	v_xor_b32_e32 v1, 1, v211
	v_pk_add_f32 v[66:67], v[68:69], v[66:67]
	v_cmp_lt_i32_e32 vcc, v1, v72
	v_pk_add_f32 v[66:67], v[70:71], v[66:67]
	s_ashr_i32 s1, s0, 31
	v_cndmask_b32_e32 v1, v211, v1, vcc
	v_add_f32_e32 v66, v66, v67
	v_lshlrev_b32_e32 v1, 2, v1
	ds_bpermute_b32 v67, v1, v66
	s_lshl_b64 s[2:3], s[0:1], 11
	v_readlane_b32 s4, v252, 20
	v_readlane_b32 s5, v252, 21
	s_add_u32 s2, s4, s2
	s_waitcnt lgkmcnt(0)
	v_add_f32_e32 v67, v66, v67
	v_xor_b32_e32 v66, 2, v211
	v_cmp_lt_i32_e32 vcc, v66, v72
	s_addc_u32 s3, s5, s3
	v_cvt_pk_bf16_f32 v70, v62, v63
	v_cvt_pk_bf16_f32 v71, v64, v65
	global_store_dwordx2 v82, v[70:71], s[2:3]
	v_cndmask_b32_e32 v66, v211, v66, vcc
	v_lshlrev_b32_e32 v66, 2, v66
	ds_bpermute_b32 v68, v66, v67
	v_cvt_pk_bf16_f32 v70, v58, v59
	v_cvt_pk_bf16_f32 v71, v60, v61
	global_store_dwordx2 v82, v[70:71], s[2:3] offset:512
	v_xor_b32_e32 v70, 32, v211
	s_waitcnt lgkmcnt(0)
	v_add_f32_e32 v67, v67, v68
	v_xor_b32_e32 v68, 4, v211
	v_cmp_lt_i32_e32 vcc, v68, v72
	s_lshl_b64 s[0:1], s[0:1], 10
	s_nop 0
	v_cndmask_b32_e32 v68, v211, v68, vcc
	v_lshlrev_b32_e32 v68, 2, v68
	ds_bpermute_b32 v69, v68, v67
	s_waitcnt lgkmcnt(0)
	v_add_f32_e32 v69, v67, v69
	v_xor_b32_e32 v67, 8, v211
	v_cmp_lt_i32_e32 vcc, v67, v72
	s_nop 1
	v_cndmask_b32_e32 v67, v211, v67, vcc
	v_lshlrev_b32_e32 v67, 2, v67
	ds_bpermute_b32 v73, v67, v69
	s_waitcnt lgkmcnt(0)
	v_add_f32_e32 v73, v69, v73
	v_xor_b32_e32 v69, 16, v211
	v_cmp_lt_i32_e32 vcc, v69, v72
	s_nop 1
	v_cndmask_b32_e32 v69, v211, v69, vcc
	v_lshlrev_b32_e32 v69, 2, v69
	ds_bpermute_b32 v74, v69, v73
	v_cmp_lt_i32_e32 vcc, v70, v72
	v_cvt_pk_bf16_f32 v72, v54, v55
	s_waitcnt lgkmcnt(0)
; #define GAS __attribute__((address_space(1)))
; __device__ __forceinline__ unsigned pk2(float lo, float hi) { unsigned r; asm("v_cvt_pk_bf16_f32 %0, %1, %2" : "=v"(r) : "v"(lo), "v"(hi)); return r; }
; __device__ __forceinline__ bf16_t* x_row_ptr(Frame& F, int row) { return (bf16_t*)(F.ws + WS_X) + (size_t)row * D; }
; __device__ __forceinline__ void n1_finish(Frame& F, int L, int row, const f32x4 (&v)[4], const f32x4 (&gs)[4], const f32x4 (&sh)[4]) {
;     bf16_t* H = (bf16_t*)(F.ws + WS_H);
;     x_store_row(x_row_ptr(F, row), F.lane, v);
;     float ss = 0.f;
; #pragma unroll
;     for (int j = 0; j < 4; ++j) ss += (v[j][0] * v[j][0] + v[j][1] * v[j][1]) + (v[j][2] * v[j][2] + v[j][3] * v[j][3]);
;     const float rinv = __builtin_amdgcn_rsqf(wave_sum(ss) * (1.0f / D) + EPS);
;     if ((L & 1) == 0) {
;         GAS unsigned* o4 = (GAS unsigned*)((unsigned char*)H + (size_t)row * D) + F.lane;
; #pragma unroll
;         for (int j = 0; j < 4; ++j) { const f32x4 h = ((v[j] * rinv) * gs[j] + sh[j]) * pg8::SC_H2; o4[64 * j] = pg8::pack4_fp8(h[0], h[1], h[2], h[3]); }
;     } else {
;         GAS u32x2* o8 = (GAS u32x2*)(H + (size_t)row * D) + F.lane;
; #pragma unroll
;         for (int j = 0; j < 4; ++j) { const f32x4 h = (v[j] * rinv) * gs[j] + sh[j]; u32x2 w; w.x = pk2(h[0], h[1]); w.y = pk2(h[2], h[3]); o8[64 * j] = w; }
;     }
; }
	v_add_f32_e32 v71, v73, v74
	v_cndmask_b32_e32 v70, v211, v70, vcc
	v_lshlrev_b32_e32 v70, 2, v70
	ds_bpermute_b32 v74, v70, v71
	v_cvt_pk_bf16_f32 v73, v56, v57
	global_store_dwordx2 v82, v[72:73], s[2:3] offset:1024
	v_cvt_pk_bf16_f32 v72, v46, v47
	v_cvt_pk_bf16_f32 v73, v48, v49
	s_waitcnt lgkmcnt(0)
	v_add_f32_e32 v71, v71, v74
	v_fmamk_f32 v71, v71, 0x3a800000, v250
	v_rsq_f32_e32 v74, v71
	v_mov_b32_e32 v71, v191
	global_store_dwordx2 v82, v[72:73], s[2:3] offset:1536
	s_add_u32 s2, s96, s0
	v_pk_mul_f32 v[62:63], v[62:63], v[74:75] op_sel_hi:[1,0]
	v_pk_mul_f32 v[64:65], v[64:65], v[74:75] op_sel_hi:[1,0]
	v_pk_fma_f32 v[62:63], v[50:51], v[62:63], v[26:27]
	v_pk_fma_f32 v[64:65], v[52:53], v[64:65], v[28:29]
	v_pk_mul_f32 v[62:63], v[62:63], s[16:17] op_sel_hi:[1,0]
	v_pk_mul_f32 v[58:59], v[58:59], v[74:75] op_sel_hi:[1,0]
	v_med3_f32 v62, v62, s15, v212
	v_med3_f32 v63, v63, s15, v212
	v_cvt_pk_fp8_f32 v71, v62, v63
	v_pk_mul_f32 v[62:63], v[64:65], s[16:17] op_sel_hi:[1,0]
	v_pk_fma_f32 v[58:59], v[42:43], v[58:59], v[22:23]
	v_med3_f32 v62, v62, s15, v212
	v_med3_f32 v63, v63, s15, v212
	v_pk_mul_f32 v[58:59], v[58:59], s[16:17] op_sel_hi:[1,0]
	v_cvt_pk_fp8_f32 v71, v62, v63 op_sel:[0,0,1]
	v_med3_f32 v58, v58, s15, v212
	v_med3_f32 v59, v59, s15, v212
	v_mov_b32_e32 v62, v191
	v_pk_mul_f32 v[60:61], v[60:61], v[74:75] op_sel_hi:[1,0]
	v_cvt_pk_fp8_f32 v62, v58, v59
	v_pk_fma_f32 v[60:61], v[44:45], v[60:61], v[24:25]
	v_pk_mul_f32 v[54:55], v[54:55], v[74:75] op_sel_hi:[1,0]
	v_pk_mul_f32 v[58:59], v[60:61], s[16:17] op_sel_hi:[1,0]
	v_pk_fma_f32 v[54:55], v[38:39], v[54:55], v[18:19]
	v_med3_f32 v58, v58, s15, v212
	v_med3_f32 v59, v59, s15, v212
	v_pk_mul_f32 v[54:55], v[54:55], s[16:17] op_sel_hi:[1,0]
	v_cvt_pk_fp8_f32 v62, v58, v59 op_sel:[0,0,1]
	v_med3_f32 v54, v54, s15, v212
	v_med3_f32 v55, v55, s15, v212
	v_mov_b32_e32 v58, v191
	v_pk_mul_f32 v[56:57], v[56:57], v[74:75] op_sel_hi:[1,0]
	v_cvt_pk_fp8_f32 v58, v54, v55
	v_pk_fma_f32 v[56:57], v[40:41], v[56:57], v[20:21]
	v_pk_mul_f32 v[46:47], v[46:47], v[74:75] op_sel_hi:[1,0]
	v_pk_mul_f32 v[54:55], v[56:57], s[16:17] op_sel_hi:[1,0]
	v_pk_fma_f32 v[46:47], v[34:35], v[46:47], v[30:31]
	v_med3_f32 v54, v54, s15, v212
	v_med3_f32 v55, v55, s15, v212
	v_pk_mul_f32 v[46:47], v[46:47], s[16:17] op_sel_hi:[1,0]
	v_cvt_pk_fp8_f32 v58, v54, v55 op_sel:[0,0,1]
	v_med3_f32 v46, v46, s15, v212
	v_med3_f32 v47, v47, s15, v212
	v_mov_b32_e32 v54, v191
	v_pk_mul_f32 v[48:49], v[48:49], v[74:75] op_sel_hi:[1,0]
	v_cvt_pk_fp8_f32 v54, v46, v47
	v_pk_fma_f32 v[48:49], v[36:37], v[48:49], v[32:33]
	s_addc_u32 s3, s97, s1
	v_pk_mul_f32 v[46:47], v[48:49], s[16:17] op_sel_hi:[1,0]
	s_add_i32 s0, s22, 1
	v_med3_f32 v46, v46, s15, v212
	v_med3_f32 v47, v47, s15, v212
	v_cvt_pk_fp8_f32 v54, v46, v47 op_sel:[0,0,1]
	v_readlane_b32 s1, v255, 22
	s_cmp_ge_i32 s0, s1
	global_store_dword v190, v71, s[2:3]
	global_store_dword v190, v62, s[2:3] offset:256
	global_store_dword v190, v58, s[2:3] offset:512
	global_store_dword v190, v54, s[2:3] offset:768
	s_cbranch_scc1 .LBB0_403
	s_add_i32 s0, s0, s38
	s_min_i32 s1, s0, 0x8000
	s_ashr_i32 s1, s1, 11
	s_cmp_eq_u32 s1, s17
	s_cbranch_scc1 .LBB0_402
	s_mul_i32 s2, s1, 0x1800
	s_ashr_i32 s3, s2, 31
	s_lshl_b64 s[2:3], s[2:3], 2
	v_readlane_b32 s1, v255, 20
	s_add_u32 s2, s1, s2
	v_readlane_b32 s1, v255, 21
	s_addc_u32 s3, s1, s3
	s_add_u32 s4, s2, 0x1000
	s_addc_u32 s5, s3, 0
	v_or_b32_e32 v18, 0x400, v84
	global_load_dwordx4 v[34:37], v84, s[4:5]
	global_load_dwordx4 v[38:41], v18, s[4:5]
	v_or_b32_e32 v18, 0x800, v84
	global_load_dwordx4 v[42:45], v18, s[4:5]
	v_or_b32_e32 v18, 0xc00, v84
	global_load_dwordx4 v[46:49], v18, s[4:5]
	v_mov_b32_e32 v85, v191
	v_lshl_add_u64 v[18:19], s[28:29], 0, v[84:85]
	flat_load_dwordx4 v[50:53], v[18:19]
	flat_load_dwordx4 v[54:57], v[18:19] offset:1024
	flat_load_dwordx4 v[58:61], v[18:19] offset:2048
	flat_load_dwordx4 v[62:65], v[18:19] offset:3072
	global_load_dwordx4 v[22:25], v84, s[2:3] offset:1024 nt
	s_nop 0
	global_load_dwordx4 v[18:21], v84, s[2:3] offset:2048 nt
	global_load_dwordx4 v[26:29], v84, s[2:3] nt
	global_load_dwordx4 v[30:33], v84, s[2:3] offset:3072 nt
	s_waitcnt vmcnt(0)
	v_pk_add_f32 v[36:37], v[36:37], 1.0 op_sel_hi:[1,0]
	v_pk_add_f32 v[34:35], v[34:35], 1.0 op_sel_hi:[1,0]
	v_pk_add_f32 v[40:41], v[40:41], 1.0 op_sel_hi:[1,0]
	v_pk_add_f32 v[38:39], v[38:39], 1.0 op_sel_hi:[1,0]
	v_pk_add_f32 v[72:73], v[44:45], 1.0 op_sel_hi:[1,0]
	v_pk_add_f32 v[74:75], v[42:43], 1.0 op_sel_hi:[1,0]
	v_pk_add_f32 v[48:49], v[48:49], 1.0 op_sel_hi:[1,0]
	v_pk_add_f32 v[46:47], v[46:47], 1.0 op_sel_hi:[1,0]
	s_waitcnt lgkmcnt(0)
	v_pk_mul_f32 v[52:53], v[52:53], v[36:37]
	v_pk_mul_f32 v[50:51], v[50:51], v[34:35]
	v_pk_mul_f32 v[44:45], v[56:57], v[40:41]
	v_pk_mul_f32 v[42:43], v[54:55], v[38:39]
	v_pk_mul_f32 v[40:41], v[60:61], v[72:73]
	v_pk_mul_f32 v[38:39], v[58:59], v[74:75]
	v_pk_mul_f32 v[36:37], v[64:65], v[48:49]
	v_pk_mul_f32 v[34:35], v[62:63], v[46:47]
